# baseline (speedup 1.0000x reference)
_Z6conv_kILi128ELi256ELi3ELi64ELi1ELi1ELb0EEvPKDF16_S1_PKfS3_PDF16_S4_S1_fS3_S3_S3_S3_:
	s_lshl_b32 s3, s2, 3
	s_load_dwordx2 s[20:21], s[0:1], 0x0
	s_load_dwordx4 s[4:7], s[0:1], 0x10
	s_load_dwordx2 s[18:19], s[0:1], 0x30
	s_and_b32 s3, s3, 56
	s_ashr_i32 s8, s2, 5
	s_add_i32 s3, s3, s8
	v_readfirstlane_b32 s27, v0
	s_lshl_b32 s8, s3, 2
	s_bfe_u32 s22, s2, 0x20003
	s_and_b32 s24, s8, 56
	s_lshr_b32 s33, s27, 6
	s_ashr_i32 s25, s3, 4
	s_and_b32 s15, s2, 32
	s_lshl_b32 s2, s22, 8
	v_bfe_u32 v24, v0, 3, 3
	v_and_b32_e32 v2, 7, v0
	s_waitcnt lgkmcnt(0)
	s_add_u32 s2, s4, s2
	v_bitop3_b32 v2, v24, v2, 6 bitop3:0x6c
	s_addc_u32 s3, s5, 0
	v_and_b32_e32 v18, 48, v0
	v_mov_b32_e32 v19, 0
	v_lshlrev_b32_e32 v20, 3, v2
	v_lshl_add_u64 v[2:3], s[2:3], 0, v[18:19]
	s_load_dword s14, s[6:7], 0x0
	global_load_dwordx4 v[14:17], v[2:3], off
	v_lshl_add_u64 v[4:5], v[2:3], 0, 64
	s_mov_b64 s[2:3], 0x80
	global_load_dwordx4 v[10:13], v[4:5], off
	v_lshl_add_u64 v[4:5], v[2:3], 0, s[2:3]
	s_mov_b64 s[2:3], 0xc0
	v_lshl_add_u64 v[2:3], v[2:3], 0, s[2:3]
	v_lshl_or_b32 v18, s33, 3, v24
	s_mov_b32 s2, 0x1e1e1e1f
	v_mul_hi_u32 v21, v18, s2
	v_lshrrev_b32_e32 v21, 2, v21
	s_movk_i32 s4, 0xffde
	s_add_i32 s12, s24, -1
	global_load_dwordx4 v[6:9], v[4:5], off
	v_mul_lo_u32 v22, v21, s4
	v_add_u32_e32 v46, s12, v21
	s_add_i32 s13, s15, -1
	s_movk_i32 s5, 0x154
	global_load_dwordx4 v[2:5], v[2:3], off
	v_add3_u32 v47, s13, v18, v22
	v_cmp_gt_u32_e32 vcc, s5, v18
	v_cmp_gt_u32_e64 s[2:3], 64, v46
	s_and_b64 s[2:3], vcc, s[2:3]
	v_cmp_gt_u32_e32 vcc, 64, v47
	v_and_b32_e32 v1, 63, v0
	s_and_b64 vcc, s[2:3], vcc
	v_mov_b64_e32 v[22:23], s[18:19]
	v_lshlrev_b32_e32 v18, 1, v20
	s_and_saveexec_b64 s[2:3], vcc
	s_lshl_b32 s6, s25, 13
	v_lshlrev_b32_e32 v21, 6, v46
	v_or3_b32 v22, v21, s6, v47
	v_ashrrev_i32_e32 v23, 31, v22
	v_lshlrev_b64 v[22:23], 7, v[22:23]
	v_lshl_add_u64 v[22:23], s[20:21], 0, v[22:23]
	v_lshl_add_u64 v[22:23], v[22:23], 0, v[18:19]
	s_or_b64 exec, exec, s[2:3]
	s_lshl_b32 s36, s33, 10
	v_lshlrev_b32_e32 v21, 4, v1
	v_or_b32_e32 v19, s36, v21
	s_add_i32 s7, s33, 8
	v_readfirstlane_b32 s2, v19
	s_mov_b32 m0, s2
	v_lshl_or_b32 v19, s7, 3, v24
	global_load_lds_dwordx4 v[22:23], off
	s_mov_b32 s6, 0x3c3c3c3d
	v_mul_hi_u32 v22, v19, s6
	v_lshrrev_b32_e32 v22, 3, v22
	v_mul_lo_u32 v23, v22, s4
	v_add_u32_e32 v48, s12, v22
	v_add3_u32 v49, s13, v19, v23
	v_cmp_gt_u32_e64 s[2:3], s5, v19
	v_cmp_gt_u32_e64 s[4:5], 64, v48
	s_and_b64 s[4:5], s[2:3], s[4:5]
	v_cmp_gt_u32_e64 s[2:3], 64, v49
	s_and_b64 s[2:3], s[4:5], s[2:3]
	v_mov_b64_e32 v[22:23], s[18:19]
	s_and_saveexec_b64 s[4:5], s[2:3]
	s_lshl_b32 s8, s25, 13
	v_lshlrev_b32_e32 v19, 6, v48
	v_or3_b32 v22, v19, s8, v49
	v_ashrrev_i32_e32 v23, 31, v22
	v_lshlrev_b64 v[22:23], 7, v[22:23]
	v_lshl_add_u64 v[22:23], s[20:21], 0, v[22:23]
	v_mov_b32_e32 v19, 0
	v_lshl_add_u64 v[22:23], v[22:23], 0, v[18:19]
	s_or_b64 exec, exec, s[4:5]
	s_lshl_b32 s37, s7, 10
	v_or_b32_e32 v19, s37, v21
	s_add_i32 s10, s33, 16
	v_readfirstlane_b32 s4, v19
	s_mov_b32 m0, s4
	v_lshl_or_b32 v19, s10, 3, v24
	global_load_lds_dwordx4 v[22:23], off
	v_mul_hi_u32 v22, v19, s6
	v_lshrrev_b32_e32 v22, 3, v22
	s_movk_i32 s8, 0xffde
	v_mul_lo_u32 v23, v22, s8
	v_add_u32_e32 v58, s12, v22
	s_movk_i32 s9, 0x154
	v_add3_u32 v59, s13, v19, v23
	v_cmp_gt_u32_e64 s[4:5], s9, v19
	v_cmp_gt_u32_e64 s[6:7], 64, v58
	s_and_b64 s[6:7], s[4:5], s[6:7]
	v_cmp_gt_u32_e64 s[4:5], 64, v59
	s_and_b64 s[4:5], s[6:7], s[4:5]
	v_mov_b64_e32 v[22:23], s[18:19]
	s_and_saveexec_b64 s[6:7], s[4:5]
	s_lshl_b32 s11, s25, 13
	v_lshlrev_b32_e32 v19, 6, v58
	v_or3_b32 v22, v19, s11, v59
	v_ashrrev_i32_e32 v23, 31, v22
	v_lshlrev_b64 v[22:23], 7, v[22:23]
	v_lshl_add_u64 v[22:23], s[20:21], 0, v[22:23]
	v_mov_b32_e32 v19, 0
	v_lshl_add_u64 v[22:23], v[22:23], 0, v[18:19]
	s_or_b64 exec, exec, s[6:7]
	s_lshl_b32 s38, s10, 10
	v_or_b32_e32 v19, s38, v21
	s_add_i32 s11, s33, 24
	v_readfirstlane_b32 s6, v19
	s_mov_b32 m0, s6
	v_lshl_or_b32 v19, s11, 3, v24
	global_load_lds_dwordx4 v[22:23], off
	s_mov_b32 s10, 0x3c3c3c3d
	v_mul_hi_u32 v22, v19, s10
	v_lshrrev_b32_e32 v22, 3, v22
	v_mul_lo_u32 v23, v22, s8
	v_add_u32_e32 v60, s12, v22
	v_add3_u32 v61, s13, v19, v23
	v_cmp_gt_u32_e64 s[6:7], s9, v19
	v_cmp_gt_u32_e64 s[8:9], 64, v60
	s_and_b64 s[8:9], s[6:7], s[8:9]
	v_cmp_gt_u32_e64 s[6:7], 64, v61
	s_and_b64 s[6:7], s[8:9], s[6:7]
	v_mov_b64_e32 v[22:23], s[18:19]
	s_and_saveexec_b64 s[8:9], s[6:7]
	s_lshl_b32 s16, s25, 13
	v_lshlrev_b32_e32 v19, 6, v60
	v_or3_b32 v22, v19, s16, v61
	v_ashrrev_i32_e32 v23, 31, v22
	v_lshlrev_b64 v[22:23], 7, v[22:23]
	v_lshl_add_u64 v[22:23], s[20:21], 0, v[22:23]
	v_mov_b32_e32 v19, 0
	v_lshl_add_u64 v[22:23], v[22:23], 0, v[18:19]
	s_or_b64 exec, exec, s[8:9]
	s_lshl_b32 s39, s11, 10
	v_or_b32_e32 v19, s39, v21
	s_add_i32 s16, s33, 32
	v_readfirstlane_b32 s8, v19
	s_mov_b32 m0, s8
	v_lshl_or_b32 v19, s16, 3, v24
	global_load_lds_dwordx4 v[22:23], off
	v_mul_hi_u32 v22, v19, s10
	v_lshrrev_b32_e32 v22, 3, v22
	s_movk_i32 s8, 0xffde
	v_mul_lo_u32 v23, v22, s8
	v_add_u32_e32 v62, s12, v22
	s_movk_i32 s8, 0x154
	v_add3_u32 v63, s13, v19, v23
	v_cmp_gt_u32_e64 s[8:9], s8, v19
	v_cmp_gt_u32_e64 s[10:11], 64, v62
	s_and_b64 s[10:11], s[8:9], s[10:11]
	v_cmp_gt_u32_e64 s[8:9], 64, v63
	s_and_b64 s[8:9], s[10:11], s[8:9]
	s_xor_b64 s[10:11], s[8:9], -1
	s_and_saveexec_b64 s[28:29], s[10:11]
	s_xor_b64 s[10:11], exec, s[28:29]
	s_lshl_b32 s17, s25, 13
	s_or_saveexec_b64 s[10:11], s[10:11]
	v_mov_b32_e32 v64, s17
	v_mov_b64_e32 v[22:23], s[18:19]
	s_xor_b64 exec, exec, s[10:11]
	s_lshl_b32 s17, s25, 13
	v_lshlrev_b32_e32 v19, 6, v62
	v_or3_b32 v22, v19, s17, v63
	v_ashrrev_i32_e32 v23, 31, v22
	v_lshlrev_b64 v[22:23], 7, v[22:23]
	v_lshl_add_u64 v[22:23], s[20:21], 0, v[22:23]
	v_mov_b32_e32 v19, 0
	v_lshl_add_u64 v[22:23], v[22:23], 0, v[18:19]
	v_mov_b32_e32 v64, s17
	s_or_b64 exec, exec, s[10:11]
	s_lshl_b32 s40, s16, 10
	v_or_b32_e32 v18, s40, v21
	s_add_i32 s23, s33, 40
	v_readfirstlane_b32 s10, v18
	s_mov_b32 m0, s10
	v_lshl_or_b32 v19, s23, 3, v24
	global_load_lds_dwordx4 v[22:23], off
	s_mov_b32 s10, 0x3c3c3c3d
	v_mul_hi_u32 v18, v19, s10
	v_lshrrev_b32_e32 v18, 3, v18
	s_movk_i32 s10, 0xffde
	s_load_dwordx2 s[16:17], s[0:1], 0x8
	v_mul_lo_u32 v22, v18, s10
	v_add_u32_e32 v18, s12, v18
	s_movk_i32 s10, 0x154
	v_add3_u32 v65, s13, v19, v22
	v_cmp_gt_u32_e64 s[10:11], s10, v19
	v_cmp_gt_u32_e64 s[12:13], 64, v18
	s_and_b64 s[12:13], s[10:11], s[12:13]
	v_cmp_gt_u32_e64 s[10:11], 64, v65
	s_and_b64 s[10:11], s[12:13], s[10:11]
	s_xor_b64 s[12:13], s[10:11], -1
	v_lshlrev_b32_e32 v66, 6, v18
	s_and_saveexec_b64 s[28:29], s[12:13]
	s_xor_b64 s[12:13], exec, s[28:29]
	v_lshlrev_b32_e32 v66, 6, v18
	s_or_saveexec_b64 s[12:13], s[12:13]
	v_mov_b64_e32 v[18:19], s[18:19]
	s_xor_b64 exec, exec, s[12:13]
	v_or3_b32 v18, v66, v64, v65
	v_ashrrev_i32_e32 v19, 31, v18
	v_lshlrev_b64 v[18:19], 7, v[18:19]
	v_lshl_add_u64 v[18:19], s[20:21], 0, v[18:19]
	v_lshlrev_b32_e32 v22, 1, v20
	v_mov_b32_e32 v23, 0
	v_lshl_add_u64 v[18:19], v[18:19], 0, v[22:23]
	s_or_b64 exec, exec, s[12:13]
	v_lshrrev_b32_e32 v129, 4, v1
	v_bitop3_b32 v23, v129, v0, 6 bitop3:0x78
	v_and_b32_e32 v128, 15, v0
	v_lshlrev_b32_e32 v23, 4, v23
	s_lshr_b32 s29, s27, 8
	v_lshl_or_b32 v23, v128, 7, v23
	v_lshl_or_b32 v23, s29, 13, v23
	s_lshl_b32 s41, s23, 10
	s_lshl_b32 s26, s22, 6
	s_and_b32 s28, s33, 3
	v_add_u32_e32 v132, 0x18000, v23
	v_or_b32_e32 v23, s41, v21
	s_lshl_b32 s22, s22, 13
	v_readfirstlane_b32 s23, v23
	s_waitcnt lgkmcnt(0)
	s_add_u32 s22, s16, s22
	s_mul_hi_u32 s44, s27, 0x38e38e39
	s_mov_b32 m0, s23
	s_addc_u32 s23, s17, 0
	s_lshr_b32 s16, s44, 10
	s_mul_i32 s16, s16, -9
	s_add_i32 s16, s16, s29
	s_mul_i32 s16, s29, 3
	s_lshl_b32 s34, s33, 11
	s_ashr_i32 s17, s16, 31
	s_add_i32 s33, s34, 0x18000
	s_lshl_b64 s[16:17], s[16:17], 15
	s_add_u32 s16, s22, s16
	s_addc_u32 s17, s23, s17
	s_mul_i32 s42, s29, -5
	s_add_i32 s42, s42, 6
	s_mul_hi_u32 s43, s42, 0xe38e38f
	v_lshl_or_b32 v22, v24, 6, s36
	s_movk_i32 s31, 0xdc0
	s_mul_i32 s43, s43, -9
	v_and_or_b32 v22, v22, s31, v20
	s_add_i32 s42, s43, s42
	global_load_lds_dwordx4 v[18:19], off
	v_lshlrev_b32_e32 v18, 1, v22
	v_mov_b32_e32 v19, 0
	s_mov_b32 m0, s33
	s_ashr_i32 s43, s42, 31
	v_lshl_add_u64 v[22:23], s[16:17], 0, v[18:19]
	global_load_lds_dwordx4 v18, s[16:17]
	s_mov_b64 s[16:17], 0x400
	s_add_i32 m0, s34, 0x18400
	s_lshl_b64 s[42:43], s[42:43], 15
	v_lshl_add_u64 v[22:23], v[22:23], 0, s[16:17]
	s_add_u32 s42, s22, s42
	global_load_lds_dwordx4 v[22:23], off
	s_addc_u32 s43, s23, s43
	s_add_i32 m0, s34, 0x1c000
	v_lshl_add_u64 v[22:23], s[42:43], 0, v[18:19]
	global_load_lds_dwordx4 v18, s[42:43]
	s_mul_i32 s42, s29, 3
	s_add_i32 s42, s42, 4
	s_mul_hi_u32 s43, s42, 0xe38e38f
	s_mul_i32 s43, s43, -9
	s_add_i32 s42, s43, s42
	s_ashr_i32 s43, s42, 31
	s_add_i32 m0, s34, 0x1c400
	s_lshl_b64 s[42:43], s[42:43], 15
	s_add_u32 s42, s22, s42
	v_lshl_add_u64 v[22:23], v[22:23], 0, s[16:17]
	s_addc_u32 s43, s23, s43
	global_load_lds_dwordx4 v[22:23], off
	s_add_i32 m0, s34, 0x20000
	v_lshl_add_u64 v[22:23], s[42:43], 0, v[18:19]
	global_load_lds_dwordx4 v18, s[42:43]
	v_lshl_add_u64 v[22:23], v[22:23], 0, s[16:17]
	s_add_i32 m0, s34, 0x20400
	s_lshr_b32 s34, s44, 9
	global_load_lds_dwordx4 v[22:23], off
	s_mul_i32 s34, s34, -9
	s_add_i32 s34, s34, s29
	s_mul_hi_i32 s42, s34, 0x55555556
	s_lshr_b32 s43, s42, 31
	s_mul_i32 s31, s28, 0x44
	s_add_i32 s42, s42, s43
	v_add_u32_e32 v130, s31, v128
	s_mul_i32 s42, s42, 31
	v_add_u32_e32 v131, 34, v130
	s_add_i32 s42, s42, s34
	s_bitcmp1_b32 s44, 9
	v_add_u32_e32 v30, s42, v130
	v_add_u32_e32 v38, s42, v131
	s_movk_i32 s42, 0x1000
	v_lshlrev_b32_e32 v68, 1, v20
	v_lshl_add_u32 v20, v48, 6, v64
	s_waitcnt vmcnt(4) lgkmcnt(0)
	s_barrier
	s_cselect_b32 s43, 0xc000, 0
	ds_read_b128 v[26:29], v132
	v_add3_u32 v48, v20, v49, s42
	v_lshl_add_u32 v20, v58, 6, v64
	ds_read_b128 v[22:25], v132 offset:2048
	v_bitop3_b32 v31, v30, v129, 6 bitop3:0x6c
	v_lshl_add_u32 v30, v30, 7, s43
	v_add3_u32 v58, v20, v59, s42
	v_lshl_add_u32 v20, v60, 6, v64
	v_lshl_or_b32 v134, v31, 4, v30
	ds_read_b128 v[34:37], v134
	v_lshl_add_u32 v46, v46, 6, v64
	v_add3_u32 v60, v20, v61, s42
	v_lshl_add_u32 v20, v62, 6, v64
	ds_read_b128 v[30:33], v134 offset:2048
	v_bitop3_b32 v39, v38, v129, 6 bitop3:0x6c
	v_lshl_add_u32 v38, v38, 7, s43
	v_add3_u32 v46, v46, v47, s42
	v_add3_u32 v62, v20, v63, s42
	v_add_u32_e32 v20, v66, v64
	v_lshl_add_u64 v[126:127], s[22:23], 0, v[18:19]
	v_add_u32_e32 v18, s36, v21
	v_lshl_or_b32 v135, v39, 4, v38
	ds_read_b128 v[42:45], v135
	v_ashrrev_i32_e32 v47, 31, v46
	v_add3_u32 v64, v20, v65, s42
	v_add_u32_e32 v136, 0xc000, v18
	v_add_u32_e32 v18, s37, v21
	s_load_dwordx2 s[12:13], s[0:1], 0x20
	ds_read_b128 v[38:41], v135 offset:2048
	v_lshlrev_b64 v[46:47], 7, v[46:47]
	v_ashrrev_i32_e32 v49, 31, v48
	v_ashrrev_i32_e32 v59, 31, v58
	v_ashrrev_i32_e32 v61, 31, v60
	v_ashrrev_i32_e32 v63, 31, v62
	v_ashrrev_i32_e32 v65, 31, v64
	v_add_u32_e32 v137, 0xc000, v18
	v_add_u32_e32 v18, s38, v21
	ds_read_b128 v[54:57], v132 offset:4096
	v_lshl_add_u64 v[46:47], s[20:21], 0, v[46:47]
	v_mov_b32_e32 v69, v19
	v_lshlrev_b64 v[48:49], 7, v[48:49]
	v_lshlrev_b64 v[58:59], 7, v[58:59]
	v_lshlrev_b64 v[60:61], 7, v[60:61]
	v_lshlrev_b64 v[62:63], 7, v[62:63]
	v_lshlrev_b64 v[64:65], 7, v[64:65]
	v_add_u32_e32 v138, 0xc000, v18
	v_add_u32_e32 v18, s39, v21
	ds_read_b128 v[50:53], v132 offset:6144
	v_lshl_add_u64 v[46:47], v[46:47], 0, v[68:69]
	v_lshl_add_u64 v[48:49], s[20:21], 0, v[48:49]
	v_lshl_add_u64 v[58:59], s[20:21], 0, v[58:59]
	v_lshl_add_u64 v[60:61], s[20:21], 0, v[60:61]
	v_lshl_add_u64 v[62:63], s[20:21], 0, v[62:63]
	v_lshl_add_u64 v[64:65], s[20:21], 0, v[64:65]
	v_mov_b32_e32 v20, s19
	v_add_u32_e32 v139, 0xc000, v18
	v_add_u32_e32 v18, s40, v21
	v_lshl_add_u64 v[48:49], v[48:49], 0, v[68:69]
	v_lshl_add_u64 v[58:59], v[58:59], 0, v[68:69]
	v_lshl_add_u64 v[60:61], v[60:61], 0, v[68:69]
	v_lshl_add_u64 v[62:63], v[62:63], 0, v[68:69]
	v_lshl_add_u64 v[64:65], v[64:65], 0, v[68:69]
	v_cndmask_b32_e32 v115, v20, v47, vcc
	v_mov_b32_e32 v47, s18
	v_add_u32_e32 v140, 0xc000, v18
	v_add_u32_e32 v18, s41, v21
	s_mov_b32 s30, 6
	v_xor_b32_e32 v133, 64, v132
	s_mov_b32 s31, 0
	s_mov_b32 s35, 1
	s_mov_b32 s34, 0xc000
	v_cndmask_b32_e32 v114, v47, v46, vcc
	v_cndmask_b32_e64 v117, v20, v49, s[2:3]
	v_cndmask_b32_e64 v116, v47, v48, s[2:3]
	v_cndmask_b32_e64 v119, v20, v59, s[4:5]
	v_cndmask_b32_e64 v118, v47, v58, s[4:5]
	v_cndmask_b32_e64 v121, v20, v61, s[6:7]
	v_cndmask_b32_e64 v120, v47, v60, s[6:7]
	v_cndmask_b32_e64 v123, v20, v63, s[8:9]
	v_cndmask_b32_e64 v122, v47, v62, s[8:9]
	v_cndmask_b32_e64 v125, v20, v65, s[10:11]
	v_cndmask_b32_e64 v124, v47, v64, s[10:11]
	s_mov_b64 s[2:3], 0
	v_add_u32_e32 v141, 0xc000, v18
	v_mov_b32_e32 v18, v19
	v_mov_b32_e32 v20, v19
	v_mov_b32_e32 v21, v19
	v_mov_b32_e32 v46, v19
	v_mov_b32_e32 v47, v19
	v_mov_b32_e32 v48, v19
	v_mov_b32_e32 v49, v19
	v_mov_b32_e32 v58, v19
	v_mov_b32_e32 v59, v19
	v_mov_b32_e32 v60, v19
	v_mov_b32_e32 v61, v19
	v_mov_b32_e32 v74, v19
	v_mov_b32_e32 v75, v19
	v_mov_b32_e32 v76, v19
	v_mov_b32_e32 v77, v19
	v_mov_b32_e32 v82, v19
	v_mov_b32_e32 v83, v19
	v_mov_b32_e32 v84, v19
	v_mov_b32_e32 v85, v19
	v_mov_b32_e32 v86, v19
	v_mov_b32_e32 v87, v19
	v_mov_b32_e32 v88, v19
	v_mov_b32_e32 v89, v19
	v_mov_b32_e32 v90, v19
	v_mov_b32_e32 v91, v19
	v_mov_b32_e32 v92, v19
	v_mov_b32_e32 v93, v19
	v_mov_b32_e32 v94, v19
	v_mov_b32_e32 v95, v19
	v_mov_b32_e32 v96, v19
	v_mov_b32_e32 v97, v19
	v_mov_b32_e32 v98, v19
	v_mov_b32_e32 v99, v19
	v_mov_b32_e32 v100, v19
	v_mov_b32_e32 v101, v19
	v_mov_b32_e32 v102, v19
	v_mov_b32_e32 v103, v19
	v_mov_b32_e32 v104, v19
	v_mov_b32_e32 v105, v19
	v_mov_b32_e32 v106, v19
	v_mov_b32_e32 v107, v19
	v_mov_b32_e32 v108, v19
	v_mov_b32_e32 v109, v19
	v_mov_b32_e32 v110, v19
	v_mov_b32_e32 v111, v19
	v_mov_b32_e32 v112, v19
	v_mov_b32_e32 v113, v19
	v_mov_b32_e32 v78, v19
	v_mov_b32_e32 v79, v19
	v_mov_b32_e32 v80, v19
	v_mov_b32_e32 v81, v19
	v_mov_b32_e32 v62, v19
	v_mov_b32_e32 v63, v19
	v_mov_b32_e32 v64, v19
	v_mov_b32_e32 v65, v19
	v_mov_b32_e32 v70, v19
	v_mov_b32_e32 v71, v19
	v_mov_b32_e32 v72, v19
	v_mov_b32_e32 v73, v19
	v_mov_b32_e32 v66, v19
	v_mov_b32_e32 v67, v19
	v_mov_b32_e32 v68, v19
	s_mov_b32 s61, 0
	s_mov_b32 s78, 0
	s_mov_b32 s67, 0
	s_mov_b32 s69, 0
	s_mov_b32 s80, 0xc000
	s_lshl_b32 s81, s29, 6
	s_lshl_b32 s79, s29, 13
	v_subrev_u32_e32 v184, s79, v132
	v_xor_b32_e32 v184, s81, v184
	v_add_u32_e32 v185, 0x2000, v184
	v_mov_b32_e32 v174, v185
	v_mov_b32_e32 v182, v130
	v_bitop3_b32 v183, v182, v129, 6 bitop3:0x6c
	v_lshl_add_u32 v182, v182, 7, 0
	v_lshl_or_b32 v176, v183, 4, v182
	v_xor_b32_e32 v176, s81, v176
	v_add_u32_e32 v182, 34, v130
	v_bitop3_b32 v183, v182, v129, 6 bitop3:0x6c
	v_lshl_add_u32 v182, v182, 7, 0
	v_lshl_or_b32 v177, v183, 4, v182
	v_xor_b32_e32 v177, s81, v177
	ds_read_b128 v[26:29], v184
	ds_read_b128 v[22:25], v184 offset:2048
	ds_read_b128 v[54:57], v184 offset:4096
	ds_read_b128 v[50:53], v184 offset:6144
	ds_read_b128 v[34:37], v176
	ds_read_b128 v[30:33], v176 offset:2048
	ds_read_b128 v[42:45], v177
	ds_read_b128 v[38:41], v177 offset:2048
	s_waitcnt lgkmcnt(0)

.Lc2_bar_0:
	s_barrier
	s_waitcnt lgkmcnt(5)
	v_mfma_f32_16x16x32_f16 v[110:113], v[26:29], v[34:37], v[110:113]
	ds_read_b128 v[142:145], v174
	s_mul_i32 s79, s29, 3
	s_add_i32 s79, s79, 2
	s_add_i32 s79, s79, s78
	s_lshl_b32 s68, s79, 15
	s_waitcnt lgkmcnt(5)
	v_mfma_f32_16x16x32_f16 v[106:109], v[22:25], v[34:37], v[106:109]
	v_add_u32_e32 v182, 68, v130
	v_bitop3_b32 v183, v182, v129, 6 bitop3:0x6c
	v_lshl_add_u32 v182, v182, 7, 0
	v_mfma_f32_16x16x32_f16 v[94:97], v[26:29], v[30:33], v[94:97]
	ds_read_b128 v[146:149], v174 offset:2048
	v_lshl_add_u64 v[178:179], v[126:127], 0, s[68:69]
	s_and_b32 s70, s34, 0xc000
	s_add_i32 s70, s70, s33
	v_mfma_f32_16x16x32_f16 v[90:93], v[22:25], v[30:33], v[90:93]
	v_lshl_or_b32 v176, v183, 4, v182
	v_xor_b32_e32 v176, s81, v176
	s_waitcnt lgkmcnt(5)
	v_mfma_f32_16x16x32_f16 v[74:77], v[26:29], v[42:45], v[74:77]
	ds_read_b128 v[150:153], v176
	v_mfma_f32_16x16x32_f16 v[58:61], v[22:25], v[42:45], v[58:61]
	v_add_u32_e32 v182, 102, v130
	v_bitop3_b32 v183, v182, v129, 6 bitop3:0x6c
	v_lshl_add_u32 v182, v182, 7, 0
	s_waitcnt lgkmcnt(5)
	v_mfma_f32_16x16x32_f16 v[78:81], v[26:29], v[38:41], v[78:81]
	ds_read_b128 v[154:157], v176 offset:2048
	v_mfma_f32_16x16x32_f16 v[62:65], v[22:25], v[38:41], v[62:65]
	v_lshl_or_b32 v177, v183, 4, v182
	v_xor_b32_e32 v177, s81, v177
	s_mov_b32 m0, s70
	s_add_i32 s71, s34, 0xffff8000
	global_load_lds_dwordx4 v[178:179], off
	s_waitcnt lgkmcnt(5)
	v_mfma_f32_16x16x32_f16 v[102:105], v[54:57], v[34:37], v[102:105]
	ds_read_b128 v[158:161], v177
	s_waitcnt lgkmcnt(5)
	v_mfma_f32_16x16x32_f16 v[98:101], v[50:53], v[34:37], v[98:101]
	s_and_b32 s71, s71, 0xc000
	s_add_i32 s72, s70, 0x400
	v_lshl_add_u64 v[180:181], v[178:179], 0, s[16:17]
	v_mfma_f32_16x16x32_f16 v[86:89], v[54:57], v[30:33], v[86:89]
	ds_read_b128 v[162:165], v177 offset:2048
	v_mfma_f32_16x16x32_f16 v[82:85], v[50:53], v[30:33], v[82:85]
	v_add_u32_e32 v175, s71, v184
	v_mfma_f32_16x16x32_f16 v[46:49], v[54:57], v[42:45], v[46:49]
	ds_read_b128 v[166:169], v174 offset:4096
	v_mfma_f32_16x16x32_f16 v[18:21], v[50:53], v[42:45], v[18:21]
	v_mfma_f32_16x16x32_f16 v[70:73], v[54:57], v[38:41], v[70:73]
	ds_read_b128 v[170:173], v174 offset:6144
	v_mfma_f32_16x16x32_f16 v[66:69], v[50:53], v[38:41], v[66:69]
	v_add_u32_e32 v174, s71, v185
	s_waitcnt lgkmcnt(7)
	v_mfma_f32_16x16x32_f16 v[110:113], v[142:145], v[42:45], v[110:113]
	ds_read_b128 v[26:29], v175
	s_waitcnt lgkmcnt(7)
	v_mfma_f32_16x16x32_f16 v[106:109], v[146:149], v[42:45], v[106:109]
	v_add_u32_e32 v182, 1, v130
	v_bitop3_b32 v183, v182, v129, 6 bitop3:0x6c
	v_lshl_add_u32 v182, v182, 7, 0
	v_mfma_f32_16x16x32_f16 v[94:97], v[142:145], v[38:41], v[94:97]
	ds_read_b128 v[22:25], v175 offset:2048
	v_mfma_f32_16x16x32_f16 v[90:93], v[146:149], v[38:41], v[90:93]
	v_lshl_or_b32 v176, v183, 4, v182
	v_xor_b32_e32 v176, s81, v176
	s_waitcnt lgkmcnt(7)
	v_mfma_f32_16x16x32_f16 v[74:77], v[142:145], v[150:153], v[74:77]
	ds_read_b128 v[34:37], v176
	v_mfma_f32_16x16x32_f16 v[58:61], v[146:149], v[150:153], v[58:61]
	s_waitcnt lgkmcnt(7)
	v_mfma_f32_16x16x32_f16 v[78:81], v[142:145], v[154:157], v[78:81]
	ds_read_b128 v[30:33], v176 offset:2048
	v_mfma_f32_16x16x32_f16 v[62:65], v[146:149], v[154:157], v[62:65]
	s_mov_b32 m0, s72
	s_addk_i32 s34, 0x4000
	global_load_lds_dwordx4 v[180:181], off
	s_waitcnt lgkmcnt(5)
	v_mfma_f32_16x16x32_f16 v[102:105], v[166:169], v[42:45], v[102:105]
	s_waitcnt lgkmcnt(4)
	v_mfma_f32_16x16x32_f16 v[98:101], v[170:173], v[42:45], v[98:101]
	v_mfma_f32_16x16x32_f16 v[86:89], v[166:169], v[38:41], v[86:89]
	v_mfma_f32_16x16x32_f16 v[82:85], v[170:173], v[38:41], v[82:85]
	v_mfma_f32_16x16x32_f16 v[46:49], v[166:169], v[150:153], v[46:49]
	ds_read_b128 v[54:57], v175 offset:4096
	v_mfma_f32_16x16x32_f16 v[18:21], v[170:173], v[150:153], v[18:21]
	v_mfma_f32_16x16x32_f16 v[70:73], v[166:169], v[154:157], v[70:73]
	ds_read_b128 v[50:53], v175 offset:6144
	v_mfma_f32_16x16x32_f16 v[66:69], v[170:173], v[154:157], v[66:69]
	v_readfirstlane_b32 s2, v136
	s_mov_b32 m0, s2
	v_readfirstlane_b32 s2, v137
	global_load_lds_dwordx4 v[114:115], off
	s_mov_b32 m0, s2
	v_readfirstlane_b32 s2, v138
	global_load_lds_dwordx4 v[116:117], off
	s_mov_b32 m0, s2
	v_readfirstlane_b32 s2, v139
	global_load_lds_dwordx4 v[118:119], off
	s_mov_b32 m0, s2
	v_readfirstlane_b32 s2, v140
	global_load_lds_dwordx4 v[120:121], off
	s_mov_b32 m0, s2
	v_readfirstlane_b32 s2, v141
	global_load_lds_dwordx4 v[122:123], off
	s_mov_b32 m0, s2
	s_mov_b64 s[2:3], -1
	global_load_lds_dwordx4 v[124:125], off
	s_mov_b32 s67, 2
	s_cmp_eq_u32 s67, 0
	s_cbranch_scc1 .Lc2_w2_1
	s_waitcnt vmcnt(8)
	s_sub_i32 s67, s67, 1
	s_branch .Lc2_bar_1

.Lc2_bar_1:
	s_barrier
	s_waitcnt lgkmcnt(5)
	v_mfma_f32_16x16x32_f16 v[110:113], v[26:29], v[150:153], v[110:113]
	ds_read_b128 v[142:145], v174
	s_mul_i32 s79, s29, 1
	s_add_i32 s79, s79, 8
	s_add_i32 s79, s79, s78
	s_lshl_b32 s68, s79, 15
	s_waitcnt lgkmcnt(5)
	v_mfma_f32_16x16x32_f16 v[106:109], v[22:25], v[150:153], v[106:109]
	v_add_u32_e32 v182, 35, v130
	v_bitop3_b32 v183, v182, v129, 6 bitop3:0x6c
	v_lshl_add_u32 v182, v182, 7, 0
	v_mfma_f32_16x16x32_f16 v[94:97], v[26:29], v[154:157], v[94:97]
	ds_read_b128 v[146:149], v174 offset:2048
	v_lshl_add_u64 v[178:179], v[126:127], 0, s[68:69]
	s_and_b32 s70, s34, 0xc000
	s_add_i32 s70, s70, s33
	v_mfma_f32_16x16x32_f16 v[90:93], v[22:25], v[154:157], v[90:93]
	v_lshl_or_b32 v176, v183, 4, v182
	v_xor_b32_e32 v176, s81, v176
	v_mfma_f32_16x16x32_f16 v[74:77], v[26:29], v[158:161], v[74:77]
	ds_read_b128 v[42:45], v176
	v_mfma_f32_16x16x32_f16 v[58:61], v[22:25], v[158:161], v[58:61]
	v_mfma_f32_16x16x32_f16 v[78:81], v[26:29], v[162:165], v[78:81]
	ds_read_b128 v[38:41], v176 offset:2048
	v_mfma_f32_16x16x32_f16 v[62:65], v[22:25], v[162:165], v[62:65]
	s_mov_b32 m0, s70
	s_add_i32 s71, s34, 0xffff8000
	global_load_lds_dwordx4 v[178:179], off
	s_waitcnt lgkmcnt(5)
	v_mfma_f32_16x16x32_f16 v[102:105], v[54:57], v[150:153], v[102:105]
	s_waitcnt lgkmcnt(4)
	v_mfma_f32_16x16x32_f16 v[98:101], v[50:53], v[150:153], v[98:101]
	s_and_b32 s71, s71, 0xc000
	s_add_i32 s72, s70, 0x400
	v_lshl_add_u64 v[180:181], v[178:179], 0, s[16:17]
	v_mfma_f32_16x16x32_f16 v[86:89], v[54:57], v[154:157], v[86:89]
	v_mfma_f32_16x16x32_f16 v[82:85], v[50:53], v[154:157], v[82:85]
	v_add_u32_e32 v175, s71, v184
	v_mfma_f32_16x16x32_f16 v[46:49], v[54:57], v[158:161], v[46:49]
	ds_read_b128 v[166:169], v174 offset:4096
	v_mfma_f32_16x16x32_f16 v[18:21], v[50:53], v[158:161], v[18:21]
	v_mfma_f32_16x16x32_f16 v[70:73], v[54:57], v[162:165], v[70:73]
	ds_read_b128 v[170:173], v174 offset:6144
	v_mfma_f32_16x16x32_f16 v[66:69], v[50:53], v[162:165], v[66:69]
	v_add_u32_e32 v174, s71, v185
	s_waitcnt lgkmcnt(5)
	v_mfma_f32_16x16x32_f16 v[110:113], v[142:145], v[34:37], v[110:113]
	ds_read_b128 v[26:29], v175
	s_waitcnt lgkmcnt(5)
	v_mfma_f32_16x16x32_f16 v[106:109], v[146:149], v[34:37], v[106:109]
	v_add_u32_e32 v182, 69, v130
	v_bitop3_b32 v183, v182, v129, 6 bitop3:0x6c
	v_lshl_add_u32 v182, v182, 7, 0
	v_mfma_f32_16x16x32_f16 v[94:97], v[142:145], v[30:33], v[94:97]
	ds_read_b128 v[22:25], v175 offset:2048
	v_mfma_f32_16x16x32_f16 v[90:93], v[146:149], v[30:33], v[90:93]
	v_lshl_or_b32 v176, v183, 4, v182
	v_xor_b32_e32 v176, s81, v176
	s_waitcnt lgkmcnt(5)
	v_mfma_f32_16x16x32_f16 v[74:77], v[142:145], v[42:45], v[74:77]
	ds_read_b128 v[150:153], v176
	v_mfma_f32_16x16x32_f16 v[58:61], v[146:149], v[42:45], v[58:61]
	v_add_u32_e32 v182, 103, v130
	v_bitop3_b32 v183, v182, v129, 6 bitop3:0x6c
	v_lshl_add_u32 v182, v182, 7, 0
	s_waitcnt lgkmcnt(5)
	v_mfma_f32_16x16x32_f16 v[78:81], v[142:145], v[38:41], v[78:81]
	ds_read_b128 v[154:157], v176 offset:2048
	v_mfma_f32_16x16x32_f16 v[62:65], v[146:149], v[38:41], v[62:65]
	v_lshl_or_b32 v177, v183, 4, v182
	v_xor_b32_e32 v177, s81, v177
	s_mov_b32 m0, s72
	s_addk_i32 s34, 0x4000
	global_load_lds_dwordx4 v[180:181], off
	s_waitcnt lgkmcnt(5)
	v_mfma_f32_16x16x32_f16 v[102:105], v[166:169], v[34:37], v[102:105]
	ds_read_b128 v[158:161], v177
	s_waitcnt lgkmcnt(5)
	v_mfma_f32_16x16x32_f16 v[98:101], v[170:173], v[34:37], v[98:101]
	v_mfma_f32_16x16x32_f16 v[86:89], v[166:169], v[30:33], v[86:89]
	ds_read_b128 v[162:165], v177 offset:2048
	v_mfma_f32_16x16x32_f16 v[82:85], v[170:173], v[30:33], v[82:85]
	v_mfma_f32_16x16x32_f16 v[46:49], v[166:169], v[42:45], v[46:49]
	ds_read_b128 v[54:57], v175 offset:4096
	v_mfma_f32_16x16x32_f16 v[18:21], v[170:173], v[42:45], v[18:21]
	v_mfma_f32_16x16x32_f16 v[70:73], v[166:169], v[38:41], v[70:73]
	ds_read_b128 v[50:53], v175 offset:6144
	v_mfma_f32_16x16x32_f16 v[66:69], v[170:173], v[38:41], v[66:69]
	s_cmp_eq_u32 s67, 0
	s_cbranch_scc1 .Lc2_w2_2
	s_waitcnt vmcnt(8)
	s_sub_i32 s67, s67, 1
	s_branch .Lc2_bar_2

.Lc2_bar_2:
	s_barrier
	s_waitcnt lgkmcnt(7)
	v_mfma_f32_16x16x32_f16 v[110:113], v[26:29], v[42:45], v[110:113]
	ds_read_b128 v[142:145], v174
	s_mul_i32 s79, s29, 3
	s_add_i32 s79, s79, 12
	s_add_i32 s79, s79, s78
	s_lshl_b32 s68, s79, 15
	s_waitcnt lgkmcnt(7)
	v_mfma_f32_16x16x32_f16 v[106:109], v[22:25], v[42:45], v[106:109]
	v_add_u32_e32 v182, 2, v130
	v_bitop3_b32 v183, v182, v129, 6 bitop3:0x6c
	v_lshl_add_u32 v182, v182, 7, 0
	v_mfma_f32_16x16x32_f16 v[94:97], v[26:29], v[38:41], v[94:97]
	ds_read_b128 v[146:149], v174 offset:2048
	v_lshl_add_u64 v[178:179], v[126:127], 0, s[68:69]
	s_and_b32 s70, s34, 0xc000
	s_add_i32 s70, s70, s33
	v_mfma_f32_16x16x32_f16 v[90:93], v[22:25], v[38:41], v[90:93]
	v_lshl_or_b32 v176, v183, 4, v182
	v_xor_b32_e32 v176, s81, v176
	s_waitcnt lgkmcnt(7)
	v_mfma_f32_16x16x32_f16 v[74:77], v[26:29], v[150:153], v[74:77]
	ds_read_b128 v[34:37], v176
	v_mfma_f32_16x16x32_f16 v[58:61], v[22:25], v[150:153], v[58:61]
	s_waitcnt lgkmcnt(7)
	v_mfma_f32_16x16x32_f16 v[78:81], v[26:29], v[154:157], v[78:81]
	ds_read_b128 v[30:33], v176 offset:2048
	v_mfma_f32_16x16x32_f16 v[62:65], v[22:25], v[154:157], v[62:65]
	s_mov_b32 m0, s70
	s_add_i32 s71, s34, 0xffff8000
	global_load_lds_dwordx4 v[178:179], off
	s_waitcnt lgkmcnt(5)
	v_mfma_f32_16x16x32_f16 v[102:105], v[54:57], v[42:45], v[102:105]
	s_waitcnt lgkmcnt(4)
	v_mfma_f32_16x16x32_f16 v[98:101], v[50:53], v[42:45], v[98:101]
	s_and_b32 s71, s71, 0xc000
	s_add_i32 s72, s70, 0x400
	v_lshl_add_u64 v[180:181], v[178:179], 0, s[16:17]
	v_mfma_f32_16x16x32_f16 v[86:89], v[54:57], v[38:41], v[86:89]
	v_mfma_f32_16x16x32_f16 v[82:85], v[50:53], v[38:41], v[82:85]
	v_add_u32_e32 v175, s71, v184
	v_mfma_f32_16x16x32_f16 v[46:49], v[54:57], v[150:153], v[46:49]
	ds_read_b128 v[166:169], v174 offset:4096
	v_mfma_f32_16x16x32_f16 v[18:21], v[50:53], v[150:153], v[18:21]
	v_mfma_f32_16x16x32_f16 v[70:73], v[54:57], v[154:157], v[70:73]
	ds_read_b128 v[170:173], v174 offset:6144
	v_mfma_f32_16x16x32_f16 v[66:69], v[50:53], v[154:157], v[66:69]
	v_add_u32_e32 v174, s71, v185
	s_waitcnt lgkmcnt(5)
	v_mfma_f32_16x16x32_f16 v[110:113], v[142:145], v[150:153], v[110:113]
	ds_read_b128 v[26:29], v175
	s_waitcnt lgkmcnt(5)
	v_mfma_f32_16x16x32_f16 v[106:109], v[146:149], v[150:153], v[106:109]
	v_add_u32_e32 v182, 36, v130
	v_bitop3_b32 v183, v182, v129, 6 bitop3:0x6c
	v_lshl_add_u32 v182, v182, 7, 0
	v_mfma_f32_16x16x32_f16 v[94:97], v[142:145], v[154:157], v[94:97]
	ds_read_b128 v[22:25], v175 offset:2048
	v_mfma_f32_16x16x32_f16 v[90:93], v[146:149], v[154:157], v[90:93]
	v_lshl_or_b32 v176, v183, 4, v182
	v_xor_b32_e32 v176, s81, v176
	v_mfma_f32_16x16x32_f16 v[74:77], v[142:145], v[158:161], v[74:77]
	ds_read_b128 v[42:45], v176
	v_mfma_f32_16x16x32_f16 v[58:61], v[146:149], v[158:161], v[58:61]
	v_mfma_f32_16x16x32_f16 v[78:81], v[142:145], v[162:165], v[78:81]
	ds_read_b128 v[38:41], v176 offset:2048
	v_mfma_f32_16x16x32_f16 v[62:65], v[146:149], v[162:165], v[62:65]
	s_mov_b32 m0, s72
	s_addk_i32 s34, 0x4000
	global_load_lds_dwordx4 v[180:181], off
	s_waitcnt lgkmcnt(5)
	v_mfma_f32_16x16x32_f16 v[102:105], v[166:169], v[150:153], v[102:105]
	s_waitcnt lgkmcnt(4)
	v_mfma_f32_16x16x32_f16 v[98:101], v[170:173], v[150:153], v[98:101]
	v_mfma_f32_16x16x32_f16 v[86:89], v[166:169], v[154:157], v[86:89]
	v_mfma_f32_16x16x32_f16 v[82:85], v[170:173], v[154:157], v[82:85]
	v_mfma_f32_16x16x32_f16 v[46:49], v[166:169], v[158:161], v[46:49]
	ds_read_b128 v[54:57], v175 offset:4096
	v_mfma_f32_16x16x32_f16 v[18:21], v[170:173], v[158:161], v[18:21]
	v_mfma_f32_16x16x32_f16 v[70:73], v[166:169], v[162:165], v[70:73]
	ds_read_b128 v[50:53], v175 offset:6144
	v_mfma_f32_16x16x32_f16 v[66:69], v[170:173], v[162:165], v[66:69]
	s_cmp_eq_u32 s67, 0
	s_cbranch_scc1 .Lc2_w2_3
	s_waitcnt vmcnt(8)
	s_sub_i32 s67, s67, 1
	s_branch .Lc2_bar_3

.Lc2_bar_3:
	s_barrier
	s_waitcnt lgkmcnt(5)
	v_mfma_f32_16x16x32_f16 v[110:113], v[26:29], v[34:37], v[110:113]
	ds_read_b128 v[142:145], v174
	s_mul_i32 s79, s29, 3
	s_add_i32 s79, s79, 10
	s_add_i32 s79, s79, s78
	s_lshl_b32 s68, s79, 15
	s_waitcnt lgkmcnt(5)
	v_mfma_f32_16x16x32_f16 v[106:109], v[22:25], v[34:37], v[106:109]
	v_add_u32_e32 v182, 70, v130
	v_bitop3_b32 v183, v182, v129, 6 bitop3:0x6c
	v_lshl_add_u32 v182, v182, 7, 0
	v_mfma_f32_16x16x32_f16 v[94:97], v[26:29], v[30:33], v[94:97]
	ds_read_b128 v[146:149], v174 offset:2048
	v_lshl_add_u64 v[178:179], v[126:127], 0, s[68:69]
	s_and_b32 s70, s34, 0xc000
	s_add_i32 s70, s70, s33
	v_mfma_f32_16x16x32_f16 v[90:93], v[22:25], v[30:33], v[90:93]
	v_lshl_or_b32 v176, v183, 4, v182
	v_xor_b32_e32 v176, s81, v176
	s_waitcnt lgkmcnt(5)
	v_mfma_f32_16x16x32_f16 v[74:77], v[26:29], v[42:45], v[74:77]
	ds_read_b128 v[150:153], v176
	v_mfma_f32_16x16x32_f16 v[58:61], v[22:25], v[42:45], v[58:61]
	v_add_u32_e32 v182, 104, v130
	v_bitop3_b32 v183, v182, v129, 6 bitop3:0x6c
	v_lshl_add_u32 v182, v182, 7, 0
	s_waitcnt lgkmcnt(5)
	v_mfma_f32_16x16x32_f16 v[78:81], v[26:29], v[38:41], v[78:81]
	ds_read_b128 v[154:157], v176 offset:2048
	v_mfma_f32_16x16x32_f16 v[62:65], v[22:25], v[38:41], v[62:65]
	v_lshl_or_b32 v177, v183, 4, v182
	v_xor_b32_e32 v177, s81, v177
	s_mov_b32 m0, s70
	s_add_i32 s71, s34, 0xffff8000
	global_load_lds_dwordx4 v[178:179], off
	s_waitcnt lgkmcnt(5)
	v_mfma_f32_16x16x32_f16 v[102:105], v[54:57], v[34:37], v[102:105]
	ds_read_b128 v[158:161], v177
	s_waitcnt lgkmcnt(5)
	v_mfma_f32_16x16x32_f16 v[98:101], v[50:53], v[34:37], v[98:101]
	s_and_b32 s71, s71, 0xc000
	s_add_i32 s72, s70, 0x400
	v_lshl_add_u64 v[180:181], v[178:179], 0, s[16:17]
	v_mfma_f32_16x16x32_f16 v[86:89], v[54:57], v[30:33], v[86:89]
	ds_read_b128 v[162:165], v177 offset:2048
	v_mfma_f32_16x16x32_f16 v[82:85], v[50:53], v[30:33], v[82:85]
	v_add_u32_e32 v175, s71, v184
	v_mfma_f32_16x16x32_f16 v[46:49], v[54:57], v[42:45], v[46:49]
	ds_read_b128 v[166:169], v174 offset:4096
	v_mfma_f32_16x16x32_f16 v[18:21], v[50:53], v[42:45], v[18:21]
	v_mfma_f32_16x16x32_f16 v[70:73], v[54:57], v[38:41], v[70:73]
	ds_read_b128 v[170:173], v174 offset:6144
	v_mfma_f32_16x16x32_f16 v[66:69], v[50:53], v[38:41], v[66:69]
	v_add_u32_e32 v174, s71, v185
	s_waitcnt lgkmcnt(7)
	v_mfma_f32_16x16x32_f16 v[110:113], v[142:145], v[42:45], v[110:113]
	ds_read_b128 v[26:29], v175
	s_waitcnt lgkmcnt(7)
	v_mfma_f32_16x16x32_f16 v[106:109], v[146:149], v[42:45], v[106:109]
	v_mov_b32_e32 v182, v130
	v_bitop3_b32 v183, v182, v129, 6 bitop3:0x6c
	v_lshl_add_u32 v182, v182, 7, s80
	v_mfma_f32_16x16x32_f16 v[94:97], v[142:145], v[38:41], v[94:97]
	ds_read_b128 v[22:25], v175 offset:2048
	v_mfma_f32_16x16x32_f16 v[90:93], v[146:149], v[38:41], v[90:93]
	v_lshl_or_b32 v176, v183, 4, v182
	v_xor_b32_e32 v176, s81, v176
	s_waitcnt lgkmcnt(7)
	v_mfma_f32_16x16x32_f16 v[74:77], v[142:145], v[150:153], v[74:77]
	ds_read_b128 v[34:37], v176
	v_mfma_f32_16x16x32_f16 v[58:61], v[146:149], v[150:153], v[58:61]
	s_waitcnt lgkmcnt(7)
	v_mfma_f32_16x16x32_f16 v[78:81], v[142:145], v[154:157], v[78:81]
	ds_read_b128 v[30:33], v176 offset:2048
	v_mfma_f32_16x16x32_f16 v[62:65], v[146:149], v[154:157], v[62:65]
	s_mov_b32 m0, s72
	s_addk_i32 s34, 0x4000
	global_load_lds_dwordx4 v[180:181], off
	s_waitcnt lgkmcnt(5)
	v_mfma_f32_16x16x32_f16 v[102:105], v[166:169], v[42:45], v[102:105]
	s_waitcnt lgkmcnt(4)
	v_mfma_f32_16x16x32_f16 v[98:101], v[170:173], v[42:45], v[98:101]
	v_mfma_f32_16x16x32_f16 v[86:89], v[166:169], v[38:41], v[86:89]
	v_mfma_f32_16x16x32_f16 v[82:85], v[170:173], v[38:41], v[82:85]
	v_mfma_f32_16x16x32_f16 v[46:49], v[166:169], v[150:153], v[46:49]
	ds_read_b128 v[54:57], v175 offset:4096
	v_mfma_f32_16x16x32_f16 v[18:21], v[170:173], v[150:153], v[18:21]
	v_mfma_f32_16x16x32_f16 v[70:73], v[166:169], v[154:157], v[70:73]
	ds_read_b128 v[50:53], v175 offset:6144
	v_mfma_f32_16x16x32_f16 v[66:69], v[170:173], v[154:157], v[66:69]
	s_cmp_eq_u32 s67, 0
	s_cbranch_scc1 .Lc2_w2_4
	s_waitcnt vmcnt(8)
	s_sub_i32 s67, s67, 1
	s_branch .Lc2_bar_4

.Lc2_bar_4:
	s_barrier
	s_waitcnt lgkmcnt(5)
	v_mfma_f32_16x16x32_f16 v[110:113], v[26:29], v[150:153], v[110:113]
	ds_read_b128 v[142:145], v174
	s_mul_i32 s79, s29, -5
	s_add_i32 s79, s79, 16
	s_add_i32 s79, s79, s78
	s_lshl_b32 s68, s79, 15
	s_waitcnt lgkmcnt(5)
	v_mfma_f32_16x16x32_f16 v[106:109], v[22:25], v[150:153], v[106:109]
	v_add_u32_e32 v182, 34, v130
	v_bitop3_b32 v183, v182, v129, 6 bitop3:0x6c
	v_lshl_add_u32 v182, v182, 7, s80
	v_mfma_f32_16x16x32_f16 v[94:97], v[26:29], v[154:157], v[94:97]
	ds_read_b128 v[146:149], v174 offset:2048
	v_lshl_add_u64 v[178:179], v[126:127], 0, s[68:69]
	s_and_b32 s70, s34, 0xc000
	s_add_i32 s70, s70, s33
	v_mfma_f32_16x16x32_f16 v[90:93], v[22:25], v[154:157], v[90:93]
	v_lshl_or_b32 v176, v183, 4, v182
	v_xor_b32_e32 v176, s81, v176
	v_mfma_f32_16x16x32_f16 v[74:77], v[26:29], v[158:161], v[74:77]
	ds_read_b128 v[42:45], v176
	v_mfma_f32_16x16x32_f16 v[58:61], v[22:25], v[158:161], v[58:61]
	v_mfma_f32_16x16x32_f16 v[78:81], v[26:29], v[162:165], v[78:81]
	ds_read_b128 v[38:41], v176 offset:2048
	v_mfma_f32_16x16x32_f16 v[62:65], v[22:25], v[162:165], v[62:65]
	s_mov_b32 m0, s70
	s_add_i32 s71, s34, 0xffff8000
	global_load_lds_dwordx4 v[178:179], off
	s_waitcnt lgkmcnt(5)
	v_mfma_f32_16x16x32_f16 v[102:105], v[54:57], v[150:153], v[102:105]
	s_waitcnt lgkmcnt(4)
	v_mfma_f32_16x16x32_f16 v[98:101], v[50:53], v[150:153], v[98:101]
	s_and_b32 s71, s71, 0xc000
	s_add_i32 s72, s70, 0x400
	v_lshl_add_u64 v[180:181], v[178:179], 0, s[16:17]
	v_mfma_f32_16x16x32_f16 v[86:89], v[54:57], v[154:157], v[86:89]
	v_mfma_f32_16x16x32_f16 v[82:85], v[50:53], v[154:157], v[82:85]
	v_add_u32_e32 v175, s71, v184
	v_mfma_f32_16x16x32_f16 v[46:49], v[54:57], v[158:161], v[46:49]
	ds_read_b128 v[166:169], v174 offset:4096
	v_mfma_f32_16x16x32_f16 v[18:21], v[50:53], v[158:161], v[18:21]
	v_mfma_f32_16x16x32_f16 v[70:73], v[54:57], v[162:165], v[70:73]
	ds_read_b128 v[170:173], v174 offset:6144
	v_mfma_f32_16x16x32_f16 v[66:69], v[50:53], v[162:165], v[66:69]
	v_add_u32_e32 v174, s71, v185
	s_waitcnt lgkmcnt(5)
	v_mfma_f32_16x16x32_f16 v[110:113], v[142:145], v[34:37], v[110:113]
	ds_read_b128 v[26:29], v175
	s_waitcnt lgkmcnt(5)
	v_mfma_f32_16x16x32_f16 v[106:109], v[146:149], v[34:37], v[106:109]
	v_add_u32_e32 v182, 68, v130
	v_bitop3_b32 v183, v182, v129, 6 bitop3:0x6c
	v_lshl_add_u32 v182, v182, 7, s80
	v_mfma_f32_16x16x32_f16 v[94:97], v[142:145], v[30:33], v[94:97]
	ds_read_b128 v[22:25], v175 offset:2048
	v_mfma_f32_16x16x32_f16 v[90:93], v[146:149], v[30:33], v[90:93]
	v_lshl_or_b32 v176, v183, 4, v182
	v_xor_b32_e32 v176, s81, v176
	s_waitcnt lgkmcnt(5)
	v_mfma_f32_16x16x32_f16 v[74:77], v[142:145], v[42:45], v[74:77]
	ds_read_b128 v[150:153], v176
	v_mfma_f32_16x16x32_f16 v[58:61], v[146:149], v[42:45], v[58:61]
	v_add_u32_e32 v182, 102, v130
	v_bitop3_b32 v183, v182, v129, 6 bitop3:0x6c
	v_lshl_add_u32 v182, v182, 7, s80
	s_waitcnt lgkmcnt(5)
	v_mfma_f32_16x16x32_f16 v[78:81], v[142:145], v[38:41], v[78:81]
	ds_read_b128 v[154:157], v176 offset:2048
	v_mfma_f32_16x16x32_f16 v[62:65], v[146:149], v[38:41], v[62:65]
	v_lshl_or_b32 v177, v183, 4, v182
	v_xor_b32_e32 v177, s81, v177
	s_mov_b32 m0, s72
	s_addk_i32 s34, 0x4000
	global_load_lds_dwordx4 v[180:181], off
	s_waitcnt lgkmcnt(5)
	v_mfma_f32_16x16x32_f16 v[102:105], v[166:169], v[34:37], v[102:105]
	ds_read_b128 v[158:161], v177
	s_waitcnt lgkmcnt(5)
	v_mfma_f32_16x16x32_f16 v[98:101], v[170:173], v[34:37], v[98:101]
	v_mfma_f32_16x16x32_f16 v[86:89], v[166:169], v[30:33], v[86:89]
	ds_read_b128 v[162:165], v177 offset:2048
	v_mfma_f32_16x16x32_f16 v[82:85], v[170:173], v[30:33], v[82:85]
	v_mfma_f32_16x16x32_f16 v[46:49], v[166:169], v[42:45], v[46:49]
	ds_read_b128 v[54:57], v175 offset:4096
	v_mfma_f32_16x16x32_f16 v[18:21], v[170:173], v[42:45], v[18:21]
	v_mfma_f32_16x16x32_f16 v[70:73], v[166:169], v[38:41], v[70:73]
	ds_read_b128 v[50:53], v175 offset:6144
	v_mfma_f32_16x16x32_f16 v[66:69], v[170:173], v[38:41], v[66:69]
	s_cmp_eq_u32 s67, 0
	s_cbranch_scc1 .Lc2_w2_5
	s_waitcnt vmcnt(8)
	s_sub_i32 s67, s67, 1
	s_branch .Lc2_bar_5

.Lc2_bar_5:
	s_barrier
	s_waitcnt lgkmcnt(7)
	v_mfma_f32_16x16x32_f16 v[110:113], v[26:29], v[42:45], v[110:113]
	ds_read_b128 v[142:145], v174
	s_mul_i32 s79, s29, 3
	s_add_i32 s79, s79, 14
	s_add_i32 s79, s79, s78
	s_lshl_b32 s68, s79, 15
	s_waitcnt lgkmcnt(7)
	v_mfma_f32_16x16x32_f16 v[106:109], v[22:25], v[42:45], v[106:109]
	v_add_u32_e32 v182, 1, v130
	v_bitop3_b32 v183, v182, v129, 6 bitop3:0x6c
	v_lshl_add_u32 v182, v182, 7, s80
	v_mfma_f32_16x16x32_f16 v[94:97], v[26:29], v[38:41], v[94:97]
	ds_read_b128 v[146:149], v174 offset:2048
	v_lshl_add_u64 v[178:179], v[126:127], 0, s[68:69]
	s_and_b32 s70, s34, 0xc000
	s_add_i32 s70, s70, s33
	v_mfma_f32_16x16x32_f16 v[90:93], v[22:25], v[38:41], v[90:93]
	v_lshl_or_b32 v176, v183, 4, v182
	v_xor_b32_e32 v176, s81, v176
	s_waitcnt lgkmcnt(7)
	v_mfma_f32_16x16x32_f16 v[74:77], v[26:29], v[150:153], v[74:77]
	ds_read_b128 v[34:37], v176
	v_mfma_f32_16x16x32_f16 v[58:61], v[22:25], v[150:153], v[58:61]
	s_waitcnt lgkmcnt(7)
	v_mfma_f32_16x16x32_f16 v[78:81], v[26:29], v[154:157], v[78:81]
	ds_read_b128 v[30:33], v176 offset:2048
	v_mfma_f32_16x16x32_f16 v[62:65], v[22:25], v[154:157], v[62:65]
	s_mov_b32 m0, s70
	s_add_i32 s71, s34, 0xffff8000
	global_load_lds_dwordx4 v[178:179], off
	s_waitcnt lgkmcnt(5)
	v_mfma_f32_16x16x32_f16 v[102:105], v[54:57], v[42:45], v[102:105]
	s_waitcnt lgkmcnt(4)
	v_mfma_f32_16x16x32_f16 v[98:101], v[50:53], v[42:45], v[98:101]
	s_and_b32 s71, s71, 0xc000
	s_add_i32 s72, s70, 0x400
	v_lshl_add_u64 v[180:181], v[178:179], 0, s[16:17]
	v_mfma_f32_16x16x32_f16 v[86:89], v[54:57], v[38:41], v[86:89]
	v_mfma_f32_16x16x32_f16 v[82:85], v[50:53], v[38:41], v[82:85]
	v_add_u32_e32 v175, s71, v184
	v_mfma_f32_16x16x32_f16 v[46:49], v[54:57], v[150:153], v[46:49]
	ds_read_b128 v[166:169], v174 offset:4096
	v_mfma_f32_16x16x32_f16 v[18:21], v[50:53], v[150:153], v[18:21]
	v_mfma_f32_16x16x32_f16 v[70:73], v[54:57], v[154:157], v[70:73]
	ds_read_b128 v[170:173], v174 offset:6144
	v_mfma_f32_16x16x32_f16 v[66:69], v[50:53], v[154:157], v[66:69]
	v_add_u32_e32 v174, s71, v185
	s_waitcnt lgkmcnt(5)
	v_mfma_f32_16x16x32_f16 v[110:113], v[142:145], v[150:153], v[110:113]
	ds_read_b128 v[26:29], v175
	s_waitcnt lgkmcnt(5)
	v_mfma_f32_16x16x32_f16 v[106:109], v[146:149], v[150:153], v[106:109]
	v_add_u32_e32 v182, 35, v130
	v_bitop3_b32 v183, v182, v129, 6 bitop3:0x6c
	v_lshl_add_u32 v182, v182, 7, s80
	v_mfma_f32_16x16x32_f16 v[94:97], v[142:145], v[154:157], v[94:97]
	ds_read_b128 v[22:25], v175 offset:2048
	v_mfma_f32_16x16x32_f16 v[90:93], v[146:149], v[154:157], v[90:93]
	v_lshl_or_b32 v176, v183, 4, v182
	v_xor_b32_e32 v176, s81, v176
	v_mfma_f32_16x16x32_f16 v[74:77], v[142:145], v[158:161], v[74:77]
	ds_read_b128 v[42:45], v176
	v_mfma_f32_16x16x32_f16 v[58:61], v[146:149], v[158:161], v[58:61]
	v_mfma_f32_16x16x32_f16 v[78:81], v[142:145], v[162:165], v[78:81]
	ds_read_b128 v[38:41], v176 offset:2048
	v_mfma_f32_16x16x32_f16 v[62:65], v[146:149], v[162:165], v[62:65]
	s_mov_b32 m0, s72
	s_addk_i32 s34, 0x4000
	global_load_lds_dwordx4 v[180:181], off
	s_waitcnt lgkmcnt(5)
	v_mfma_f32_16x16x32_f16 v[102:105], v[166:169], v[150:153], v[102:105]
	s_waitcnt lgkmcnt(4)
	v_mfma_f32_16x16x32_f16 v[98:101], v[170:173], v[150:153], v[98:101]
	v_mfma_f32_16x16x32_f16 v[86:89], v[166:169], v[154:157], v[86:89]
	v_mfma_f32_16x16x32_f16 v[82:85], v[170:173], v[154:157], v[82:85]
	v_mfma_f32_16x16x32_f16 v[46:49], v[166:169], v[158:161], v[46:49]
	ds_read_b128 v[54:57], v175 offset:4096
	v_mfma_f32_16x16x32_f16 v[18:21], v[170:173], v[158:161], v[18:21]
	v_mfma_f32_16x16x32_f16 v[70:73], v[166:169], v[162:165], v[70:73]
	ds_read_b128 v[50:53], v175 offset:6144
	v_mfma_f32_16x16x32_f16 v[66:69], v[170:173], v[162:165], v[66:69]
	s_cmp_eq_u32 s67, 0
	s_cbranch_scc1 .Lc2_w2_6
	s_waitcnt vmcnt(8)
	s_sub_i32 s67, s67, 1
	s_branch .Lc2_bar_6

.Lc2_bar_6:
	s_barrier
	s_waitcnt lgkmcnt(5)
	v_mfma_f32_16x16x32_f16 v[110:113], v[26:29], v[34:37], v[110:113]
	ds_read_b128 v[142:145], v174
	s_mul_i32 s79, s29, 3
	s_add_i32 s79, s79, 18
	s_add_i32 s79, s79, s78
	s_lshl_b32 s68, s79, 15
	s_waitcnt lgkmcnt(5)
	v_mfma_f32_16x16x32_f16 v[106:109], v[22:25], v[34:37], v[106:109]
	v_add_u32_e32 v182, 69, v130
	v_bitop3_b32 v183, v182, v129, 6 bitop3:0x6c
	v_lshl_add_u32 v182, v182, 7, s80
	v_mfma_f32_16x16x32_f16 v[94:97], v[26:29], v[30:33], v[94:97]
	ds_read_b128 v[146:149], v174 offset:2048
	v_lshl_add_u64 v[178:179], v[126:127], 0, s[68:69]
	s_and_b32 s70, s34, 0xc000
	s_add_i32 s70, s70, s33
	v_mfma_f32_16x16x32_f16 v[90:93], v[22:25], v[30:33], v[90:93]
	v_lshl_or_b32 v176, v183, 4, v182
	v_xor_b32_e32 v176, s81, v176
	s_waitcnt lgkmcnt(5)
	v_mfma_f32_16x16x32_f16 v[74:77], v[26:29], v[42:45], v[74:77]
	ds_read_b128 v[150:153], v176
	v_mfma_f32_16x16x32_f16 v[58:61], v[22:25], v[42:45], v[58:61]
	v_add_u32_e32 v182, 103, v130
	v_bitop3_b32 v183, v182, v129, 6 bitop3:0x6c
	v_lshl_add_u32 v182, v182, 7, s80
	s_waitcnt lgkmcnt(5)
	v_mfma_f32_16x16x32_f16 v[78:81], v[26:29], v[38:41], v[78:81]
	ds_read_b128 v[154:157], v176 offset:2048
	v_mfma_f32_16x16x32_f16 v[62:65], v[22:25], v[38:41], v[62:65]
	v_lshl_or_b32 v177, v183, 4, v182
	v_xor_b32_e32 v177, s81, v177
	s_mov_b32 m0, s70
	s_add_i32 s71, s34, 0xffff8000
	global_load_lds_dwordx4 v[178:179], off
	s_waitcnt lgkmcnt(5)
	v_mfma_f32_16x16x32_f16 v[102:105], v[54:57], v[34:37], v[102:105]
	ds_read_b128 v[158:161], v177
	s_waitcnt lgkmcnt(5)
	v_mfma_f32_16x16x32_f16 v[98:101], v[50:53], v[34:37], v[98:101]
	s_and_b32 s71, s71, 0xc000
	s_add_i32 s72, s70, 0x400
	v_lshl_add_u64 v[180:181], v[178:179], 0, s[16:17]
	v_mfma_f32_16x16x32_f16 v[86:89], v[54:57], v[30:33], v[86:89]
	ds_read_b128 v[162:165], v177 offset:2048
	v_mfma_f32_16x16x32_f16 v[82:85], v[50:53], v[30:33], v[82:85]
	v_add_u32_e32 v175, s71, v184
	v_mfma_f32_16x16x32_f16 v[46:49], v[54:57], v[42:45], v[46:49]
	ds_read_b128 v[166:169], v174 offset:4096
	v_mfma_f32_16x16x32_f16 v[18:21], v[50:53], v[42:45], v[18:21]
	v_mfma_f32_16x16x32_f16 v[70:73], v[54:57], v[38:41], v[70:73]
	ds_read_b128 v[170:173], v174 offset:6144
	v_mfma_f32_16x16x32_f16 v[66:69], v[50:53], v[38:41], v[66:69]
	v_add_u32_e32 v174, s71, v185
	s_waitcnt lgkmcnt(7)
	v_mfma_f32_16x16x32_f16 v[110:113], v[142:145], v[42:45], v[110:113]
	ds_read_b128 v[26:29], v175
	s_waitcnt lgkmcnt(7)
	v_mfma_f32_16x16x32_f16 v[106:109], v[146:149], v[42:45], v[106:109]
	v_add_u32_e32 v182, 2, v130
	v_bitop3_b32 v183, v182, v129, 6 bitop3:0x6c
	v_lshl_add_u32 v182, v182, 7, s80
	v_mfma_f32_16x16x32_f16 v[94:97], v[142:145], v[38:41], v[94:97]
	ds_read_b128 v[22:25], v175 offset:2048
	v_mfma_f32_16x16x32_f16 v[90:93], v[146:149], v[38:41], v[90:93]
	v_lshl_or_b32 v176, v183, 4, v182
	v_xor_b32_e32 v176, s81, v176
	s_waitcnt lgkmcnt(7)
	v_mfma_f32_16x16x32_f16 v[74:77], v[142:145], v[150:153], v[74:77]
	ds_read_b128 v[34:37], v176
	v_mfma_f32_16x16x32_f16 v[58:61], v[146:149], v[150:153], v[58:61]
	s_waitcnt lgkmcnt(7)
	v_mfma_f32_16x16x32_f16 v[78:81], v[142:145], v[154:157], v[78:81]
	ds_read_b128 v[30:33], v176 offset:2048
	v_mfma_f32_16x16x32_f16 v[62:65], v[146:149], v[154:157], v[62:65]
	s_mov_b32 m0, s72
	s_addk_i32 s34, 0x4000
	global_load_lds_dwordx4 v[180:181], off
	s_waitcnt lgkmcnt(5)
	v_mfma_f32_16x16x32_f16 v[102:105], v[166:169], v[42:45], v[102:105]
	s_waitcnt lgkmcnt(4)
	v_mfma_f32_16x16x32_f16 v[98:101], v[170:173], v[42:45], v[98:101]
	v_mfma_f32_16x16x32_f16 v[86:89], v[166:169], v[38:41], v[86:89]
	v_mfma_f32_16x16x32_f16 v[82:85], v[170:173], v[38:41], v[82:85]
	v_mfma_f32_16x16x32_f16 v[46:49], v[166:169], v[150:153], v[46:49]
	ds_read_b128 v[54:57], v175 offset:4096
	v_mfma_f32_16x16x32_f16 v[18:21], v[170:173], v[150:153], v[18:21]
	v_mfma_f32_16x16x32_f16 v[70:73], v[166:169], v[154:157], v[70:73]
	ds_read_b128 v[50:53], v175 offset:6144
	v_mfma_f32_16x16x32_f16 v[66:69], v[170:173], v[154:157], v[66:69]
	s_cmp_eq_u32 s67, 0
	s_cbranch_scc1 .Lc2_w2_7
	s_waitcnt vmcnt(8)
	s_sub_i32 s67, s67, 1
	s_branch .Lc2_bar_7

.Lc2_bar_7:
	s_barrier
	s_waitcnt lgkmcnt(5)
	v_mfma_f32_16x16x32_f16 v[110:113], v[26:29], v[150:153], v[110:113]
	ds_read_b128 v[142:145], v174
	s_mul_i32 s79, s29, -5
	s_add_i32 s79, s79, 24
	s_add_i32 s79, s79, s78
	s_lshl_b32 s68, s79, 15
	s_waitcnt lgkmcnt(5)
	v_mfma_f32_16x16x32_f16 v[106:109], v[22:25], v[150:153], v[106:109]
	v_add_u32_e32 v182, 36, v130
	v_bitop3_b32 v183, v182, v129, 6 bitop3:0x6c
	v_lshl_add_u32 v182, v182, 7, s80
	v_mfma_f32_16x16x32_f16 v[94:97], v[26:29], v[154:157], v[94:97]
	ds_read_b128 v[146:149], v174 offset:2048
	v_lshl_add_u64 v[178:179], v[126:127], 0, s[68:69]
	s_and_b32 s70, s34, 0xc000
	s_add_i32 s70, s70, s33
	v_mfma_f32_16x16x32_f16 v[90:93], v[22:25], v[154:157], v[90:93]
	v_lshl_or_b32 v176, v183, 4, v182
	v_xor_b32_e32 v176, s81, v176
	v_mfma_f32_16x16x32_f16 v[74:77], v[26:29], v[158:161], v[74:77]
	ds_read_b128 v[42:45], v176
	v_mfma_f32_16x16x32_f16 v[58:61], v[22:25], v[158:161], v[58:61]
	v_mfma_f32_16x16x32_f16 v[78:81], v[26:29], v[162:165], v[78:81]
	ds_read_b128 v[38:41], v176 offset:2048
	v_mfma_f32_16x16x32_f16 v[62:65], v[22:25], v[162:165], v[62:65]
	s_mov_b32 m0, s70
	s_add_i32 s71, s34, 0xffff8000
	global_load_lds_dwordx4 v[178:179], off
	s_waitcnt lgkmcnt(5)
	v_mfma_f32_16x16x32_f16 v[102:105], v[54:57], v[150:153], v[102:105]
	s_waitcnt lgkmcnt(4)
	v_mfma_f32_16x16x32_f16 v[98:101], v[50:53], v[150:153], v[98:101]
	s_and_b32 s71, s71, 0xc000
	s_add_i32 s72, s70, 0x400
	v_lshl_add_u64 v[180:181], v[178:179], 0, s[16:17]
	v_mfma_f32_16x16x32_f16 v[86:89], v[54:57], v[154:157], v[86:89]
	v_mfma_f32_16x16x32_f16 v[82:85], v[50:53], v[154:157], v[82:85]
	v_add_u32_e32 v175, s71, v184
	v_mfma_f32_16x16x32_f16 v[46:49], v[54:57], v[158:161], v[46:49]
	ds_read_b128 v[166:169], v174 offset:4096
	v_mfma_f32_16x16x32_f16 v[18:21], v[50:53], v[158:161], v[18:21]
	v_mfma_f32_16x16x32_f16 v[70:73], v[54:57], v[162:165], v[70:73]
	ds_read_b128 v[170:173], v174 offset:6144
	v_mfma_f32_16x16x32_f16 v[66:69], v[50:53], v[162:165], v[66:69]
	v_add_u32_e32 v174, s71, v185
	s_waitcnt lgkmcnt(5)
	v_mfma_f32_16x16x32_f16 v[110:113], v[142:145], v[34:37], v[110:113]
	ds_read_b128 v[26:29], v175
	s_waitcnt lgkmcnt(5)
	v_mfma_f32_16x16x32_f16 v[106:109], v[146:149], v[34:37], v[106:109]
	v_add_u32_e32 v182, 70, v130
	v_bitop3_b32 v183, v182, v129, 6 bitop3:0x6c
	v_lshl_add_u32 v182, v182, 7, s80
	v_mfma_f32_16x16x32_f16 v[94:97], v[142:145], v[30:33], v[94:97]
	ds_read_b128 v[22:25], v175 offset:2048
	v_mfma_f32_16x16x32_f16 v[90:93], v[146:149], v[30:33], v[90:93]
	v_lshl_or_b32 v176, v183, 4, v182
	v_xor_b32_e32 v176, s81, v176
	s_waitcnt lgkmcnt(5)
	v_mfma_f32_16x16x32_f16 v[74:77], v[142:145], v[42:45], v[74:77]
	ds_read_b128 v[150:153], v176
	v_mfma_f32_16x16x32_f16 v[58:61], v[146:149], v[42:45], v[58:61]
	v_add_u32_e32 v182, 104, v130
	v_bitop3_b32 v183, v182, v129, 6 bitop3:0x6c
	v_lshl_add_u32 v182, v182, 7, s80
	s_waitcnt lgkmcnt(5)
	v_mfma_f32_16x16x32_f16 v[78:81], v[142:145], v[38:41], v[78:81]
	ds_read_b128 v[154:157], v176 offset:2048
	v_mfma_f32_16x16x32_f16 v[62:65], v[146:149], v[38:41], v[62:65]
	v_lshl_or_b32 v177, v183, 4, v182
	v_xor_b32_e32 v177, s81, v177
	s_mov_b32 m0, s72
	s_addk_i32 s34, 0x4000
	global_load_lds_dwordx4 v[180:181], off
	s_waitcnt lgkmcnt(5)
	v_mfma_f32_16x16x32_f16 v[102:105], v[166:169], v[34:37], v[102:105]
	ds_read_b128 v[158:161], v177
	s_waitcnt lgkmcnt(5)
	v_mfma_f32_16x16x32_f16 v[98:101], v[170:173], v[34:37], v[98:101]
	v_mfma_f32_16x16x32_f16 v[86:89], v[166:169], v[30:33], v[86:89]
	ds_read_b128 v[162:165], v177 offset:2048
	v_mfma_f32_16x16x32_f16 v[82:85], v[170:173], v[30:33], v[82:85]
	v_mfma_f32_16x16x32_f16 v[46:49], v[166:169], v[42:45], v[46:49]
	ds_read_b128 v[54:57], v175 offset:4096
	v_mfma_f32_16x16x32_f16 v[18:21], v[170:173], v[42:45], v[18:21]
	v_mfma_f32_16x16x32_f16 v[70:73], v[166:169], v[38:41], v[70:73]
	ds_read_b128 v[50:53], v175 offset:6144
	v_mfma_f32_16x16x32_f16 v[66:69], v[170:173], v[38:41], v[66:69]
	s_cmp_eq_u32 s67, 0
	s_cbranch_scc1 .Lc2_w2_8
	s_waitcnt vmcnt(8)
	s_sub_i32 s67, s67, 1
	s_branch .Lc2_bar_8

.Lc2_bar_8:
	s_barrier
	s_waitcnt lgkmcnt(7)
	v_mfma_f32_16x16x32_f16 v[110:113], v[26:29], v[42:45], v[110:113]
	ds_read_b128 v[142:145], v174
	s_mul_i32 s79, s29, 3
	s_add_i32 s79, s79, 22
	s_add_i32 s79, s79, s78
	s_lshl_b32 s68, s79, 15
	s_waitcnt lgkmcnt(7)
	v_mfma_f32_16x16x32_f16 v[106:109], v[22:25], v[42:45], v[106:109]
	v_mov_b32_e32 v182, v130
	v_bitop3_b32 v183, v182, v129, 6 bitop3:0x6c
	v_lshl_add_u32 v182, v182, 7, 0
	v_mfma_f32_16x16x32_f16 v[94:97], v[26:29], v[38:41], v[94:97]
	ds_read_b128 v[146:149], v174 offset:2048
	v_lshl_add_u64 v[178:179], v[126:127], 0, s[68:69]
	s_and_b32 s70, s34, 0xc000
	s_add_i32 s70, s70, s33
	v_mfma_f32_16x16x32_f16 v[90:93], v[22:25], v[38:41], v[90:93]
	v_lshl_or_b32 v176, v183, 4, v182
	v_xor_b32_e32 v176, s81, v176
	s_waitcnt lgkmcnt(7)
	v_mfma_f32_16x16x32_f16 v[74:77], v[26:29], v[150:153], v[74:77]
	ds_read_b128 v[34:37], v176
	v_mfma_f32_16x16x32_f16 v[58:61], v[22:25], v[150:153], v[58:61]
	s_waitcnt lgkmcnt(7)
	v_mfma_f32_16x16x32_f16 v[78:81], v[26:29], v[154:157], v[78:81]
	ds_read_b128 v[30:33], v176 offset:2048
	v_mfma_f32_16x16x32_f16 v[62:65], v[22:25], v[154:157], v[62:65]
	s_mov_b32 m0, s70
	s_add_i32 s71, s34, 0xffff8000
	global_load_lds_dwordx4 v[178:179], off
	s_waitcnt lgkmcnt(5)
	v_mfma_f32_16x16x32_f16 v[102:105], v[54:57], v[42:45], v[102:105]
	s_waitcnt lgkmcnt(4)
	v_mfma_f32_16x16x32_f16 v[98:101], v[50:53], v[42:45], v[98:101]
	s_and_b32 s71, s71, 0xc000
	s_add_i32 s72, s70, 0x400
	v_lshl_add_u64 v[180:181], v[178:179], 0, s[16:17]
	v_mfma_f32_16x16x32_f16 v[86:89], v[54:57], v[38:41], v[86:89]
	v_mfma_f32_16x16x32_f16 v[82:85], v[50:53], v[38:41], v[82:85]
	v_add_u32_e32 v175, s71, v184
	v_mfma_f32_16x16x32_f16 v[46:49], v[54:57], v[150:153], v[46:49]
	ds_read_b128 v[166:169], v174 offset:4096
	v_mfma_f32_16x16x32_f16 v[18:21], v[50:53], v[150:153], v[18:21]
	v_mfma_f32_16x16x32_f16 v[70:73], v[54:57], v[154:157], v[70:73]
	ds_read_b128 v[170:173], v174 offset:6144
	v_mfma_f32_16x16x32_f16 v[66:69], v[50:53], v[154:157], v[66:69]
	v_add_u32_e32 v174, s71, v185
	s_waitcnt lgkmcnt(5)
	v_mfma_f32_16x16x32_f16 v[110:113], v[142:145], v[150:153], v[110:113]
	ds_read_b128 v[26:29], v175
	s_waitcnt lgkmcnt(5)
	v_mfma_f32_16x16x32_f16 v[106:109], v[146:149], v[150:153], v[106:109]
	v_add_u32_e32 v182, 34, v130
	v_bitop3_b32 v183, v182, v129, 6 bitop3:0x6c
	v_lshl_add_u32 v182, v182, 7, 0
	v_mfma_f32_16x16x32_f16 v[94:97], v[142:145], v[154:157], v[94:97]
	ds_read_b128 v[22:25], v175 offset:2048
	v_mfma_f32_16x16x32_f16 v[90:93], v[146:149], v[154:157], v[90:93]
	v_lshl_or_b32 v176, v183, 4, v182
	v_xor_b32_e32 v176, s81, v176
	v_mfma_f32_16x16x32_f16 v[74:77], v[142:145], v[158:161], v[74:77]
	ds_read_b128 v[42:45], v176
	v_mfma_f32_16x16x32_f16 v[58:61], v[146:149], v[158:161], v[58:61]
	v_mfma_f32_16x16x32_f16 v[78:81], v[142:145], v[162:165], v[78:81]
	ds_read_b128 v[38:41], v176 offset:2048
	v_mfma_f32_16x16x32_f16 v[62:65], v[146:149], v[162:165], v[62:65]
	s_mov_b32 m0, s72
	s_addk_i32 s34, 0x4000
	global_load_lds_dwordx4 v[180:181], off
	s_waitcnt lgkmcnt(5)
	v_mfma_f32_16x16x32_f16 v[102:105], v[166:169], v[150:153], v[102:105]
	s_waitcnt lgkmcnt(4)
	v_mfma_f32_16x16x32_f16 v[98:101], v[170:173], v[150:153], v[98:101]
	v_mfma_f32_16x16x32_f16 v[86:89], v[166:169], v[154:157], v[86:89]
	v_mfma_f32_16x16x32_f16 v[82:85], v[170:173], v[154:157], v[82:85]
	v_mfma_f32_16x16x32_f16 v[46:49], v[166:169], v[158:161], v[46:49]
	ds_read_b128 v[54:57], v175 offset:4096
	v_mfma_f32_16x16x32_f16 v[18:21], v[170:173], v[158:161], v[18:21]
	s_add_i32 s61, s61, 1
	s_add_i32 s78, s78, 18
	v_mfma_f32_16x16x32_f16 v[70:73], v[166:169], v[162:165], v[70:73]
	ds_read_b128 v[50:53], v175 offset:6144
	s_cmp_eq_u32 s61, 1
	v_mfma_f32_16x16x32_f16 v[66:69], v[170:173], v[162:165], v[66:69]
	s_cbranch_scc0 .Lc2_loop

	.amdhsa_kernel _Z6conv_kILi128ELi256ELi3ELi64ELi1ELi1ELb0EEvPKDF16_S1_PKfS3_PDF16_S4_S1_fS3_S3_S3_S3_
		.amdhsa_group_segment_fixed_size 163840
		.amdhsa_private_segment_fixed_size 0
		.amdhsa_kernarg_size 96
		.amdhsa_user_sgpr_count 2
		.amdhsa_user_sgpr_dispatch_ptr 0
		.amdhsa_user_sgpr_queue_ptr 0
		.amdhsa_user_sgpr_kernarg_segment_ptr 1
		.amdhsa_user_sgpr_dispatch_id 0
		.amdhsa_user_sgpr_kernarg_preload_length 0
		.amdhsa_user_sgpr_kernarg_preload_offset 0
		.amdhsa_user_sgpr_private_segment_size 0
		.amdhsa_uses_dynamic_stack 0
		.amdhsa_enable_private_segment 0
		.amdhsa_system_sgpr_workgroup_id_x 1
		.amdhsa_system_sgpr_workgroup_id_y 0
		.amdhsa_system_sgpr_workgroup_id_z 0
		.amdhsa_system_sgpr_workgroup_info 0
		.amdhsa_system_vgpr_workitem_id 0
		.amdhsa_next_free_vgpr 188
		.amdhsa_next_free_sgpr 96
		.amdhsa_accum_offset 188
		.amdhsa_reserve_vcc 1
		.amdhsa_float_round_mode_32 0
		.amdhsa_float_round_mode_16_64 0
		.amdhsa_float_denorm_mode_32 3
		.amdhsa_float_denorm_mode_16_64 3
		.amdhsa_dx10_clamp 1
		.amdhsa_ieee_mode 1
		.amdhsa_fp16_overflow 0
		.amdhsa_tg_split 0
		.amdhsa_exception_fp_ieee_invalid_op 0
		.amdhsa_exception_fp_denorm_src 0
		.amdhsa_exception_fp_ieee_div_zero 0
		.amdhsa_exception_fp_ieee_overflow 0
		.amdhsa_exception_fp_ieee_underflow 0
		.amdhsa_exception_fp_ieee_inexact 0
		.amdhsa_exception_int_div_zero 0
	.end_amdhsa_kernel

amdhsa.kernels:
  - .agpr_count:     0
    .args:
      - .actual_access:  read_only
        .address_space:  global
        .offset:         0
        .size:           8
        .value_kind:     global_buffer
      - .actual_access:  read_only
        .address_space:  global
        .offset:         8
        .size:           8
        .value_kind:     global_buffer
      - .actual_access:  read_only
        .address_space:  global
        .offset:         16
        .size:           8
        .value_kind:     global_buffer
      - .actual_access:  read_only
        .address_space:  global
        .offset:         24
        .size:           8
        .value_kind:     global_buffer
      - .actual_access:  read_only
        .address_space:  global
        .offset:         32
        .size:           8
        .value_kind:     global_buffer
      - .actual_access:  read_only
        .address_space:  global
        .offset:         40
        .size:           8
        .value_kind:     global_buffer
      - .actual_access:  write_only
        .address_space:  global
        .offset:         48
        .size:           8
        .value_kind:     global_buffer
      - .actual_access:  write_only
        .address_space:  global
        .offset:         56
        .size:           8
        .value_kind:     global_buffer
      - .actual_access:  write_only
        .address_space:  global
        .offset:         64
        .size:           8
        .value_kind:     global_buffer
      - .actual_access:  write_only
        .address_space:  global
        .offset:         72
        .size:           8
        .value_kind:     global_buffer
      - .actual_access:  write_only
        .address_space:  global
        .offset:         80
        .size:           8
        .value_kind:     global_buffer
      - .actual_access:  write_only
        .address_space:  global
        .offset:         88
        .size:           8
        .value_kind:     global_buffer
      - .actual_access:  read_only
        .address_space:  global
        .offset:         96
        .size:           8
        .value_kind:     global_buffer
      - .actual_access:  read_only
        .address_space:  global
        .offset:         104
        .size:           8
        .value_kind:     global_buffer
      - .actual_access:  read_only
        .address_space:  global
        .offset:         112
        .size:           8
        .value_kind:     global_buffer
      - .actual_access:  read_only
        .address_space:  global
        .offset:         120
        .size:           8
        .value_kind:     global_buffer
      - .actual_access:  write_only
        .address_space:  global
        .offset:         128
        .size:           8
        .value_kind:     global_buffer
      - .actual_access:  write_only
        .address_space:  global
        .offset:         136
        .size:           8
        .value_kind:     global_buffer
    .group_segment_fixed_size: 14400
    .kernarg_segment_align: 8
    .kernarg_segment_size: 144
    .language:       OpenCL C
    .language_version:
      - 2
      - 0
    .max_flat_workgroup_size: 256
    .name:           _Z10prep_all_kPKfS0_S0_S0_S0_S0_PDF16_S1_S1_S1_S1_S1_S0_S0_S0_S0_S1_Pj
    .private_segment_fixed_size: 0
    .sgpr_count:     27
    .sgpr_spill_count: 0
    .symbol:         _Z10prep_all_kPKfS0_S0_S0_S0_S0_PDF16_S1_S1_S1_S1_S1_S0_S0_S0_S0_S1_Pj.kd
    .uniform_work_group_size: 1
    .uses_dynamic_stack: false
    .vgpr_count:     64
    .vgpr_spill_count: 0
    .wavefront_size: 64
  - .agpr_count:     0
    .args:
      - .actual_access:  read_only
        .address_space:  global
        .offset:         0
        .size:           8
        .value_kind:     global_buffer
      - .actual_access:  read_only
        .address_space:  global
        .offset:         8
        .size:           8
        .value_kind:     global_buffer
      - .actual_access:  read_only
        .address_space:  global
        .offset:         16
        .size:           8
        .value_kind:     global_buffer
      - .actual_access:  read_only
        .address_space:  global
        .offset:         24
        .size:           8
        .value_kind:     global_buffer
      - .actual_access:  read_only
        .address_space:  global
        .offset:         32
        .size:           8
        .value_kind:     global_buffer
      - .actual_access:  read_only
        .address_space:  global
        .offset:         40
        .size:           8
        .value_kind:     global_buffer
      - .actual_access:  write_only
        .address_space:  global
        .offset:         48
        .size:           8
        .value_kind:     global_buffer
    .group_segment_fixed_size: 0
    .kernarg_segment_align: 8
    .kernarg_segment_size: 56
    .language:       OpenCL C
    .language_version:
      - 2
      - 0
    .max_flat_workgroup_size: 256
    .name:           _Z9finish6_kPKDF16_PKfS2_S2_S2_S2_Pf
    .private_segment_fixed_size: 0
    .sgpr_count:     18
    .sgpr_spill_count: 0
    .symbol:         _Z9finish6_kPKDF16_PKfS2_S2_S2_S2_Pf.kd
    .uniform_work_group_size: 1
    .uses_dynamic_stack: false
    .vgpr_count:     51
    .vgpr_spill_count: 0
    .wavefront_size: 64
  - .agpr_count:     0
    .args:
      - .actual_access:  read_only
        .address_space:  global
        .offset:         0
        .size:           8
        .value_kind:     global_buffer
      - .actual_access:  write_only
        .address_space:  global
        .offset:         8
        .size:           8
        .value_kind:     global_buffer
    .group_segment_fixed_size: 16640
    .kernarg_segment_align: 8
    .kernarg_segment_size: 16
    .language:       OpenCL C
    .language_version:
      - 2
      - 0
    .max_flat_workgroup_size: 256
    .name:           _Z6gram_kPKfPf
    .private_segment_fixed_size: 0
    .sgpr_count:     16
    .sgpr_spill_count: 0
    .symbol:         _Z6gram_kPKfPf.kd
    .uniform_work_group_size: 1
    .uses_dynamic_stack: false
    .vgpr_count:     38
    .vgpr_spill_count: 0
    .wavefront_size: 64
  - .agpr_count:     0
    .args:
      - .actual_access:  read_only
        .address_space:  global
        .offset:         0
        .size:           8
        .value_kind:     global_buffer
      - .address_space:  global
        .offset:         8
        .size:           8
        .value_kind:     global_buffer
      - .actual_access:  read_only
        .address_space:  global
        .offset:         16
        .size:           8
        .value_kind:     global_buffer
      - .actual_access:  read_only
        .address_space:  global
        .offset:         24
        .size:           8
        .value_kind:     global_buffer
      - .actual_access:  read_only
        .address_space:  global
        .offset:         32
        .size:           8
        .value_kind:     global_buffer
      - .actual_access:  write_only
        .address_space:  global
        .offset:         40
        .size:           8
        .value_kind:     global_buffer
      - .actual_access:  read_only
        .address_space:  global
        .offset:         48
        .size:           8
        .value_kind:     global_buffer
      - .offset:         56
        .size:           4
        .value_kind:     by_value
      - .actual_access:  read_only
        .address_space:  global
        .offset:         64
        .size:           8
        .value_kind:     global_buffer
      - .actual_access:  read_only
        .address_space:  global
        .offset:         72
        .size:           8
        .value_kind:     global_buffer
      - .actual_access:  read_only
        .address_space:  global
        .offset:         80
        .size:           8
        .value_kind:     global_buffer
      - .actual_access:  read_only
        .address_space:  global
        .offset:         88
        .size:           8
        .value_kind:     global_buffer
    .group_segment_fixed_size: 147456
    .kernarg_segment_align: 8
    .kernarg_segment_size: 96
    .language:       OpenCL C
    .language_version:
      - 2
      - 0
    .max_flat_workgroup_size: 512
    .name:           _Z6conv_kILi64ELi128ELi20ELi128ELi4ELi4ELb1EEvPKDF16_S1_PKfS3_PDF16_S4_S1_fS3_S3_S3_S3_
    .private_segment_fixed_size: 0
    .sgpr_count:     43
    .sgpr_spill_count: 0
    .symbol:         _Z6conv_kILi64ELi128ELi20ELi128ELi4ELi4ELb1EEvPKDF16_S1_PKfS3_PDF16_S4_S1_fS3_S3_S3_S3_.kd
    .uniform_work_group_size: 1
    .uses_dynamic_stack: false
    .vgpr_count:     160
    .vgpr_spill_count: 0
    .wavefront_size: 64
  - .agpr_count:     0
    .args:
      - .actual_access:  read_only
        .address_space:  global
        .offset:         0
        .size:           8
        .value_kind:     global_buffer
      - .actual_access:  read_only
        .address_space:  global
        .offset:         8
        .size:           8
        .value_kind:     global_buffer
      - .actual_access:  read_only
        .address_space:  global
        .offset:         16
        .size:           8
        .value_kind:     global_buffer
      - .actual_access:  write_only
        .address_space:  global
        .offset:         24
        .size:           8
        .value_kind:     global_buffer
    .group_segment_fixed_size: 0
    .kernarg_segment_align: 8
    .kernarg_segment_size: 32
    .language:       OpenCL C
    .language_version:
      - 2
      - 0
    .max_flat_workgroup_size: 256
    .name:           _Z8finish_kILi128ELi4EEvPKDF16_PKfS3_PDF16_
    .private_segment_fixed_size: 0
    .sgpr_count:     18
    .sgpr_spill_count: 0
    .symbol:         _Z8finish_kILi128ELi4EEvPKDF16_PKfS3_PDF16_.kd
    .uniform_work_group_size: 1
    .uses_dynamic_stack: false
    .vgpr_count:     44
    .vgpr_spill_count: 0
    .wavefront_size: 64
  - .agpr_count:     0
    .args:
      - .address_space:  global
        .offset:         0
        .size:           8
        .value_kind:     global_buffer
      - .address_space:  global
        .offset:         8
        .size:           8
        .value_kind:     global_buffer
      - .address_space:  global
        .offset:         16
        .size:           8
        .value_kind:     global_buffer
      - .actual_access:  read_only
        .address_space:  global
        .offset:         24
        .size:           8
        .value_kind:     global_buffer
      - .actual_access:  write_only
        .address_space:  global
        .offset:         32
        .size:           8
        .value_kind:     global_buffer
      - .actual_access:  read_only
        .address_space:  global
        .offset:         40
        .size:           8
        .value_kind:     global_buffer
      - .address_space:  global
        .offset:         48
        .size:           8
        .value_kind:     global_buffer
      - .offset:         56
        .size:           4
        .value_kind:     by_value
      - .actual_access:  read_only
        .address_space:  global
        .offset:         64
        .size:           8
        .value_kind:     global_buffer
      - .actual_access:  read_only
        .address_space:  global
        .offset:         72
        .size:           8
        .value_kind:     global_buffer
      - .actual_access:  read_only
        .address_space:  global
        .offset:         80
        .size:           8
        .value_kind:     global_buffer
      - .actual_access:  read_only
        .address_space:  global
        .offset:         88
        .size:           8
        .value_kind:     global_buffer
    .group_segment_fixed_size: 163840
    .kernarg_segment_align: 8
    .kernarg_segment_size: 96
    .language:       OpenCL C
    .language_version:
      - 2
      - 0
    .max_flat_workgroup_size: 512
    .name:           _Z6conv_kILi128ELi256ELi3ELi64ELi1ELi1ELb0EEvPKDF16_S1_PKfS3_PDF16_S4_S1_fS3_S3_S3_S3_
    .private_segment_fixed_size: 0
    .sgpr_count:     51
    .sgpr_spill_count: 0
    .symbol:         _Z6conv_kILi128ELi256ELi3ELi64ELi1ELi1ELb0EEvPKDF16_S1_PKfS3_PDF16_S4_S1_fS3_S3_S3_S3_.kd
    .uniform_work_group_size: 1
    .uses_dynamic_stack: false
    .vgpr_count:     188
    .vgpr_spill_count: 0
    .wavefront_size: 64
  - .agpr_count:     0
    .args:
      - .address_space:  global
        .offset:         0
        .size:           8
        .value_kind:     global_buffer
      - .address_space:  global
        .offset:         8
        .size:           8
        .value_kind:     global_buffer
      - .address_space:  global
        .offset:         16
        .size:           8
        .value_kind:     global_buffer
      - .actual_access:  read_only
        .address_space:  global
        .offset:         24
        .size:           8
        .value_kind:     global_buffer
      - .actual_access:  write_only
        .address_space:  global
        .offset:         32
        .size:           8
        .value_kind:     global_buffer
      - .actual_access:  read_only
        .address_space:  global
        .offset:         40
        .size:           8
        .value_kind:     global_buffer
      - .address_space:  global
        .offset:         48
        .size:           8
        .value_kind:     global_buffer
      - .offset:         56
        .size:           4
        .value_kind:     by_value
      - .actual_access:  read_only
        .address_space:  global
        .offset:         64
        .size:           8
        .value_kind:     global_buffer
      - .actual_access:  read_only
        .address_space:  global
        .offset:         72
        .size:           8
        .value_kind:     global_buffer
      - .actual_access:  read_only
        .address_space:  global
        .offset:         80
        .size:           8
        .value_kind:     global_buffer
      - .actual_access:  read_only
        .address_space:  global
        .offset:         88
        .size:           8
        .value_kind:     global_buffer
    .group_segment_fixed_size: 163840
    .kernarg_segment_align: 8
    .kernarg_segment_size: 96
    .language:       OpenCL C
    .language_version:
      - 2
      - 0
    .max_flat_workgroup_size: 512
    .name:           _Z6conv_kILi256ELi512ELi3ELi128ELi1ELi1ELb0EEvPKDF16_S1_PKfS3_PDF16_S4_S1_fS3_S3_S3_S3_
    .private_segment_fixed_size: 0
    .sgpr_count:     64
    .sgpr_spill_count: 0
    .symbol:         _Z6conv_kILi256ELi512ELi3ELi128ELi1ELi1ELb0EEvPKDF16_S1_PKfS3_PDF16_S4_S1_fS3_S3_S3_S3_.kd
    .uniform_work_group_size: 1
    .uses_dynamic_stack: false
    .vgpr_count:     184
    .vgpr_spill_count: 0
    .wavefront_size: 64
  - .agpr_count:     0
    .args:
      - .address_space:  global
        .offset:         0
        .size:           8
        .value_kind:     global_buffer
      - .address_space:  global
        .offset:         8
        .size:           8
        .value_kind:     global_buffer
      - .address_space:  global
        .offset:         16
        .size:           8
        .value_kind:     global_buffer
      - .actual_access:  read_only
        .address_space:  global
        .offset:         24
        .size:           8
        .value_kind:     global_buffer
      - .actual_access:  write_only
        .address_space:  global
        .offset:         32
        .size:           8
        .value_kind:     global_buffer
      - .actual_access:  read_only
        .address_space:  global
        .offset:         40
        .size:           8
        .value_kind:     global_buffer
      - .address_space:  global
        .offset:         48
        .size:           8
        .value_kind:     global_buffer
      - .offset:         56
        .size:           4
        .value_kind:     by_value
      - .actual_access:  read_only
        .address_space:  global
        .offset:         64
        .size:           8
        .value_kind:     global_buffer
      - .actual_access:  read_only
        .address_space:  global
        .offset:         72
        .size:           8
        .value_kind:     global_buffer
      - .actual_access:  read_only
        .address_space:  global
        .offset:         80
        .size:           8
        .value_kind:     global_buffer
      - .actual_access:  read_only
        .address_space:  global
        .offset:         88
        .size:           8
        .value_kind:     global_buffer
    .group_segment_fixed_size: 163840
    .kernarg_segment_align: 8
    .kernarg_segment_size: 96
    .language:       OpenCL C
    .language_version:
      - 2
      - 0
    .max_flat_workgroup_size: 512
    .name:           _Z6conv_kILi512ELi256ELi3ELi64ELi1ELi1ELb0EEvPKDF16_S1_PKfS3_PDF16_S4_S1_fS3_S3_S3_S3_
    .private_segment_fixed_size: 0
    .sgpr_count:     66
    .sgpr_spill_count: 0
    .symbol:         _Z6conv_kILi512ELi256ELi3ELi64ELi1ELi1ELb0EEvPKDF16_S1_PKfS3_PDF16_S4_S1_fS3_S3_S3_S3_.kd
    .uniform_work_group_size: 1
    .uses_dynamic_stack: false
    .vgpr_count:     208
    .vgpr_spill_count: 0
    .wavefront_size: 64
  - .agpr_count:     0
    .args:
      - .address_space:  global
        .offset:         0
        .size:           8
        .value_kind:     global_buffer
      - .address_space:  global
        .offset:         8
        .size:           8
        .value_kind:     global_buffer
      - .actual_access:  read_only
        .address_space:  global
        .offset:         16
        .size:           8
        .value_kind:     global_buffer
      - .actual_access:  read_only
        .address_space:  global
        .offset:         24
        .size:           8
        .value_kind:     global_buffer
      - .actual_access:  read_only
        .address_space:  global
        .offset:         32
        .size:           8
        .value_kind:     global_buffer
      - .actual_access:  write_only
        .address_space:  global
        .offset:         40
        .size:           8
        .value_kind:     global_buffer
      - .address_space:  global
        .offset:         48
        .size:           8
        .value_kind:     global_buffer
      - .offset:         56
        .size:           4
        .value_kind:     by_value
      - .actual_access:  read_only
        .address_space:  global
        .offset:         64
        .size:           8
        .value_kind:     global_buffer
      - .actual_access:  read_only
        .address_space:  global
        .offset:         72
        .size:           8
        .value_kind:     global_buffer
      - .actual_access:  read_only
        .address_space:  global
        .offset:         80
        .size:           8
        .value_kind:     global_buffer
      - .actual_access:  read_only
        .address_space:  global
        .offset:         88
        .size:           8
        .value_kind:     global_buffer
    .group_segment_fixed_size: 163840
    .kernarg_segment_align: 8
    .kernarg_segment_size: 96
    .language:       OpenCL C
    .language_version:
      - 2
      - 0
    .max_flat_workgroup_size: 512
    .name:           _Z6conv_kILi256ELi128ELi3ELi64ELi1ELi2ELb0EEvPKDF16_S1_PKfS3_PDF16_S4_S1_fS3_S3_S3_S3_
    .private_segment_fixed_size: 0
    .sgpr_count:     55
    .sgpr_spill_count: 0
    .symbol:         _Z6conv_kILi256ELi128ELi3ELi64ELi1ELi2ELb0EEvPKDF16_S1_PKfS3_PDF16_S4_S1_fS3_S3_S3_S3_.kd
    .uniform_work_group_size: 1
    .uses_dynamic_stack: false
    .vgpr_count:     172
    .vgpr_spill_count: 0
    .wavefront_size: 64
  - .agpr_count:     0
    .args:
      - .actual_access:  read_only
        .address_space:  global
        .offset:         0
        .size:           8
        .value_kind:     global_buffer
      - .actual_access:  read_only
        .address_space:  global
        .offset:         8
        .size:           8
        .value_kind:     global_buffer
      - .actual_access:  read_only
        .address_space:  global
        .offset:         16
        .size:           8
        .value_kind:     global_buffer
      - .actual_access:  write_only
        .address_space:  global
        .offset:         24
        .size:           8
        .value_kind:     global_buffer
    .group_segment_fixed_size: 0
    .kernarg_segment_align: 8
    .kernarg_segment_size: 32
    .language:       OpenCL C
    .language_version:
      - 2
      - 0
    .max_flat_workgroup_size: 256
    .name:           _Z8finish_kILi128ELi2EEvPKDF16_PKfS3_PDF16_
    .private_segment_fixed_size: 0
    .sgpr_count:     18
    .sgpr_spill_count: 0
    .symbol:         _Z8finish_kILi128ELi2EEvPKDF16_PKfS3_PDF16_.kd
    .uniform_work_group_size: 1
    .uses_dynamic_stack: false
    .vgpr_count:     28
    .vgpr_spill_count: 0
    .wavefront_size: 64
  - .agpr_count:     0
    .args:
      - .address_space:  global
        .offset:         0
        .size:           8
        .value_kind:     global_buffer
      - .address_space:  global
        .offset:         8
        .size:           8
        .value_kind:     global_buffer
      - .actual_access:  read_only
        .address_space:  global
        .offset:         16
        .size:           8
        .value_kind:     global_buffer
      - .actual_access:  read_only
        .address_space:  global
        .offset:         24
        .size:           8
        .value_kind:     global_buffer
      - .actual_access:  read_only
        .address_space:  global
        .offset:         32
        .size:           8
        .value_kind:     global_buffer
      - .actual_access:  write_only
        .address_space:  global
        .offset:         40
        .size:           8
        .value_kind:     global_buffer
      - .address_space:  global
        .offset:         48
        .size:           8
        .value_kind:     global_buffer
      - .offset:         56
        .size:           4
        .value_kind:     by_value
      - .actual_access:  read_only
        .address_space:  global
        .offset:         64
        .size:           8
        .value_kind:     global_buffer
      - .actual_access:  read_only
        .address_space:  global
        .offset:         72
        .size:           8
        .value_kind:     global_buffer
      - .actual_access:  read_only
        .address_space:  global
        .offset:         80
        .size:           8
        .value_kind:     global_buffer
      - .actual_access:  read_only
        .address_space:  global
        .offset:         88
        .size:           8
        .value_kind:     global_buffer
    .group_segment_fixed_size: 147456
    .kernarg_segment_align: 8
    .kernarg_segment_size: 96
    .language:       OpenCL C
    .language_version:
      - 2
      - 0
    .max_flat_workgroup_size: 512
    .name:           _Z6conv_kILi128ELi64ELi20ELi64ELi4ELi4ELb0EEvPKDF16_S1_PKfS3_PDF16_S4_S1_fS3_S3_S3_S3_
    .private_segment_fixed_size: 0
    .sgpr_count:     64
    .sgpr_spill_count: 0
    .symbol:         _Z6conv_kILi128ELi64ELi20ELi64ELi4ELi4ELb0EEvPKDF16_S1_PKfS3_PDF16_S4_S1_fS3_S3_S3_S3_.kd
    .uniform_work_group_size: 1
    .uses_dynamic_stack: false
    .vgpr_count:     184
    .vgpr_spill_count: 0
    .wavefront_size: 64
